# GEMM K-loops: A- and B-fragment LDS reads (with their address adds) of the next phase issued between the current phase's MFMAs
# baseline (speedup 1.0000x reference)
.LBB0_191:
	s_ashr_i32 s61, s60, 31
	s_lshl_b64 s[62:63], s[60:61], 19
	s_add_u32 s62, s12, s62
	s_addc_u32 s63, s13, s63
	s_ashr_i32 s59, s58, 31
	s_lshl_b64 s[64:65], s[58:59], 19
	s_add_u32 s64, s14, s64
	s_addc_u32 s65, s15, s65
	s_andn2_b64 vcc, exec, s[30:31]
	s_cbranch_vccnz .LBB0_195
	v_cmp_lt_i64_e32 vcc, s[68:69], v[142:143]
	s_and_b64 s[68:69], vcc, exec
	s_cselect_b32 s9, s63, s11
	s_cselect_b32 s59, s62, s10
	s_cselect_b32 s61, s65, s67
	s_cselect_b32 s86, s64, s66
	s_add_u32 s10, s10, 0x40080
	s_addc_u32 s11, s11, 0
	s_add_u32 s87, s66, 0x100
	s_addc_u32 s88, s67, 0
	s_mov_b32 s66, 0
	s_waitcnt vmcnt(0)
	v_add_u32_e32 v154, s77, v157
	ds_read_b128 v[146:149], v154
	ds_read_b128 v[150:153], v154 offset:1024
	ds_read_b128 v[164:167], v154 offset:2048
	ds_read_b128 v[168:171], v154 offset:3072
	s_add_i32 s89, s66, 2
	s_add_u32 s67, s10, 0xfffc0080
	s_addc_u32 s68, s11, -1
	s_cmp_eq_u32 s75, s66
	s_cselect_b32 s66, s86, s87
	s_cselect_b32 s69, s9, s68
	s_cselect_b32 s68, s59, s67
	s_cselect_b32 s67, s61, s88
	v_lshl_add_u64 v[206:207], s[10:11], 0, v[138:139]
	s_add_i32 m0, s52, 0xc000
	ds_read_b128 v[172:175], v159
	ds_read_b128 v[176:179], v159 offset:1024
	ds_read_b128 v[180:183], v159 offset:2048
	ds_read_b128 v[184:187], v159 offset:3072
	ds_read_b128 v[188:191], v159 offset:4096
	ds_read_b128 v[192:195], v159 offset:5120
	ds_read_b128 v[198:201], v159 offset:6144
	ds_read_b128 v[202:205], v159 offset:7168
	global_load_lds_dwordx4 v[206:207], off
	v_lshl_add_u64 v[206:207], s[10:11], 0, v[140:141]
	s_add_i32 m0, s52, 0xe000
	s_nop 0
	global_load_lds_dwordx4 v[206:207], off
	s_waitcnt lgkmcnt(8)
	s_barrier
	s_waitcnt lgkmcnt(0)
	s_setprio 1
	s_waitcnt lgkmcnt(0)
	v_mfma_i32_16x16x64_i8 v[62:65], v[146:149], v[172:175], 0
	v_add_u32_e32 v154, s78, v157
	ds_read_b128 v[218:221], v154 offset:3072
	ds_read_b128 v[214:217], v154 offset:2048
	ds_read_b128 v[210:213], v154 offset:1024
	ds_read_b128 v[206:209], v154
	v_mfma_i32_16x16x64_i8 v[58:61], v[164:167], v[172:175], 0
	v_mfma_i32_16x16x64_i8 v[54:57], v[146:149], v[180:183], 0
	v_mfma_i32_16x16x64_i8 v[50:53], v[164:167], v[180:183], 0
	v_mfma_i32_16x16x64_i8 v[46:49], v[146:149], v[188:191], 0
	v_mfma_i32_16x16x64_i8 v[42:45], v[164:167], v[188:191], 0
	v_mfma_i32_16x16x64_i8 v[38:41], v[146:149], v[198:201], 0
	v_mfma_i32_16x16x64_i8 v[34:37], v[164:167], v[198:201], 0
	v_mfma_i32_16x16x64_i8 v[62:65], v[150:153], v[176:179], v[62:65]
	v_mfma_i32_16x16x64_i8 v[58:61], v[168:171], v[176:179], v[58:61]
	v_mfma_i32_16x16x64_i8 v[54:57], v[150:153], v[184:187], v[54:57]
	v_mfma_i32_16x16x64_i8 v[50:53], v[168:171], v[184:187], v[50:53]
	v_mfma_i32_16x16x64_i8 v[46:49], v[150:153], v[192:195], v[46:49]
	v_mfma_i32_16x16x64_i8 v[42:45], v[168:171], v[192:195], v[42:45]
	v_mfma_i32_16x16x64_i8 v[38:41], v[150:153], v[202:205], v[38:41]
	v_mfma_i32_16x16x64_i8 v[34:37], v[168:171], v[202:205], v[34:37]
	s_setprio 0
	s_barrier
	s_add_i32 s90, s77, s4
	v_lshl_add_u64 v[222:223], s[66:67], 0, v[134:135]
	s_mov_b32 m0, s90
	global_load_lds_dwordx4 v[222:223], off
	v_lshl_add_u64 v[224:225], s[66:67], 0, v[130:131]
	s_add_i32 m0, s90, 0x2000
	s_nop 0
	global_load_lds_dwordx4 v[224:225], off
	s_barrier
	s_waitcnt lgkmcnt(0)
	s_setprio 1
	s_waitcnt lgkmcnt(0)
	v_mfma_i32_16x16x64_i8 v[126:129], v[206:209], v[172:175], 0
	v_mfma_i32_16x16x64_i8 v[122:125], v[214:217], v[172:175], 0
	ds_read_b128 v[172:175], v159 offset:16384
	v_mfma_i32_16x16x64_i8 v[118:121], v[206:209], v[180:183], 0
	v_mfma_i32_16x16x64_i8 v[114:117], v[214:217], v[180:183], 0
	ds_read_b128 v[180:183], v159 offset:18432
	v_mfma_i32_16x16x64_i8 v[110:113], v[206:209], v[188:191], 0
	v_mfma_i32_16x16x64_i8 v[106:109], v[214:217], v[188:191], 0
	ds_read_b128 v[188:191], v159 offset:20480
	v_mfma_i32_16x16x64_i8 v[102:105], v[206:209], v[198:201], 0
	v_mfma_i32_16x16x64_i8 v[98:101], v[214:217], v[198:201], 0
	ds_read_b128 v[198:201], v159 offset:22528
	v_mfma_i32_16x16x64_i8 v[126:129], v[210:213], v[176:179], v[126:129]
	v_mfma_i32_16x16x64_i8 v[122:125], v[218:221], v[176:179], v[122:125]
	ds_read_b128 v[176:179], v159 offset:17408
	v_mfma_i32_16x16x64_i8 v[118:121], v[210:213], v[184:187], v[118:121]
	v_mfma_i32_16x16x64_i8 v[114:117], v[218:221], v[184:187], v[114:117]
	ds_read_b128 v[184:187], v159 offset:19456
	v_mfma_i32_16x16x64_i8 v[110:113], v[210:213], v[192:195], v[110:113]
	v_mfma_i32_16x16x64_i8 v[106:109], v[218:221], v[192:195], v[106:109]
	ds_read_b128 v[192:195], v159 offset:21504
	v_mfma_i32_16x16x64_i8 v[102:105], v[210:213], v[202:205], v[102:105]
	v_mfma_i32_16x16x64_i8 v[98:101], v[218:221], v[202:205], v[98:101]
	ds_read_b128 v[202:205], v159 offset:23552
	s_setprio 0
	s_mov_b32 m0, s52
	v_lshl_add_u64 v[226:227], s[68:69], 0, v[136:137]
	s_barrier
	global_load_lds_dwordx4 v[226:227], off
	v_lshl_add_u64 v[228:229], s[68:69], 0, v[132:133]
	s_mov_b32 m0, s53
	s_nop 0
	global_load_lds_dwordx4 v[228:229], off
	s_barrier
	s_waitcnt lgkmcnt(0)
	s_setprio 1
	s_waitcnt lgkmcnt(0)
	v_mfma_i32_16x16x64_i8 v[30:33], v[146:149], v[172:175], 0
	v_mfma_i32_16x16x64_i8 v[26:29], v[164:167], v[172:175], 0
	v_mfma_i32_16x16x64_i8 v[22:25], v[146:149], v[180:183], 0
	v_mfma_i32_16x16x64_i8 v[18:21], v[164:167], v[180:183], 0
	v_mfma_i32_16x16x64_i8 v[14:17], v[146:149], v[188:191], 0
	v_mfma_i32_16x16x64_i8 v[10:13], v[164:167], v[188:191], 0
	v_mfma_i32_16x16x64_i8 v[6:9], v[146:149], v[198:201], 0
	v_mfma_i32_16x16x64_i8 v[2:5], v[164:167], v[198:201], 0
	v_mfma_i32_16x16x64_i8 v[30:33], v[150:153], v[176:179], v[30:33]
	v_mfma_i32_16x16x64_i8 v[26:29], v[168:171], v[176:179], v[26:29]
	v_mfma_i32_16x16x64_i8 v[22:25], v[150:153], v[184:187], v[22:25]
	v_mfma_i32_16x16x64_i8 v[18:21], v[168:171], v[184:187], v[18:21]
	v_mfma_i32_16x16x64_i8 v[14:17], v[150:153], v[192:195], v[14:17]
	v_mfma_i32_16x16x64_i8 v[10:13], v[168:171], v[192:195], v[10:13]
	v_mfma_i32_16x16x64_i8 v[6:9], v[150:153], v[202:205], v[6:9]
	v_mfma_i32_16x16x64_i8 v[2:5], v[168:171], v[202:205], v[2:5]
	s_setprio 0
	s_barrier
	s_add_u32 s90, s66, 0x40000
	s_addc_u32 s91, s67, 0
	s_add_i32 s92, s78, s4
	v_lshl_add_u64 v[146:147], s[90:91], 0, v[134:135]
	s_mov_b32 m0, s92
	s_nop 0
	global_load_lds_dwordx4 v[146:147], off
	v_lshl_add_u64 v[146:147], s[90:91], 0, v[130:131]
	s_add_i32 m0, s92, 0x2000
	s_nop 0
	global_load_lds_dwordx4 v[146:147], off
	s_waitcnt vmcnt(6)
	s_barrier
	s_setprio 1
	v_mfma_i32_16x16x64_i8 v[94:97], v[206:209], v[172:175], 0
	v_mfma_i32_16x16x64_i8 v[90:93], v[214:217], v[172:175], 0
	ds_read_b128 v[172:175], v159 offset:32768
	v_mfma_i32_16x16x64_i8 v[86:89], v[206:209], v[180:183], 0
	v_mfma_i32_16x16x64_i8 v[82:85], v[214:217], v[180:183], 0
	ds_read_b128 v[180:183], v159 offset:34816
	v_mfma_i32_16x16x64_i8 v[78:81], v[206:209], v[188:191], 0
	v_mfma_i32_16x16x64_i8 v[74:77], v[214:217], v[188:191], 0
	ds_read_b128 v[188:191], v159 offset:36864
	v_mfma_i32_16x16x64_i8 v[70:73], v[206:209], v[198:201], 0
	v_mfma_i32_16x16x64_i8 v[66:69], v[214:217], v[198:201], 0
	ds_read_b128 v[198:201], v159 offset:38912
	v_mfma_i32_16x16x64_i8 v[94:97], v[210:213], v[176:179], v[94:97]
	v_mfma_i32_16x16x64_i8 v[90:93], v[218:221], v[176:179], v[90:93]
	ds_read_b128 v[176:179], v159 offset:33792
	v_mfma_i32_16x16x64_i8 v[86:89], v[210:213], v[184:187], v[86:89]
	v_mfma_i32_16x16x64_i8 v[82:85], v[218:221], v[184:187], v[82:85]
	ds_read_b128 v[184:187], v159 offset:35840
	v_mfma_i32_16x16x64_i8 v[78:81], v[210:213], v[192:195], v[78:81]
	v_mfma_i32_16x16x64_i8 v[74:77], v[218:221], v[192:195], v[74:77]
	ds_read_b128 v[192:195], v159 offset:37888
	v_mfma_i32_16x16x64_i8 v[70:73], v[210:213], v[202:205], v[70:73]
	v_mfma_i32_16x16x64_i8 v[66:69], v[218:221], v[202:205], v[66:69]
	ds_read_b128 v[202:205], v159 offset:39936
	s_setprio 0
	s_add_i32 s90, 0, 0x18000
	v_add_u32_e32 v154, s90, v157
	s_barrier
	ds_read_b128 v[146:149], v154
	ds_read_b128 v[150:153], v154 offset:1024
	ds_read_b128 v[164:167], v154 offset:2048
	ds_read_b128 v[168:171], v154 offset:3072
	s_add_u32 s68, s68, 0x40000
	s_addc_u32 s69, s69, 0
	s_mov_b32 m0, s54
	v_lshl_add_u64 v[206:207], s[68:69], 0, v[136:137]
	global_load_lds_dwordx4 v[206:207], off
	v_lshl_add_u64 v[206:207], s[68:69], 0, v[132:133]
	s_mov_b32 m0, s55
	s_nop 0
	global_load_lds_dwordx4 v[206:207], off
	s_waitcnt lgkmcnt(8)
	s_barrier
	s_waitcnt lgkmcnt(0)
	s_setprio 1
	s_waitcnt lgkmcnt(0)
	v_mfma_i32_16x16x64_i8 v[62:65], v[146:149], v[172:175], v[62:65]
	v_mfma_i32_16x16x64_i8 v[58:61], v[164:167], v[172:175], v[58:61]
	v_mfma_i32_16x16x64_i8 v[54:57], v[146:149], v[180:183], v[54:57]
	v_mfma_i32_16x16x64_i8 v[50:53], v[164:167], v[180:183], v[50:53]
	v_mfma_i32_16x16x64_i8 v[46:49], v[146:149], v[188:191], v[46:49]
	v_mfma_i32_16x16x64_i8 v[42:45], v[164:167], v[188:191], v[42:45]
	v_mfma_i32_16x16x64_i8 v[38:41], v[146:149], v[198:201], v[38:41]
	v_mfma_i32_16x16x64_i8 v[34:37], v[164:167], v[198:201], v[34:37]
	v_mfma_i32_16x16x64_i8 v[62:65], v[150:153], v[176:179], v[62:65]
	v_mfma_i32_16x16x64_i8 v[58:61], v[168:171], v[176:179], v[58:61]
	v_mfma_i32_16x16x64_i8 v[54:57], v[150:153], v[184:187], v[54:57]
	v_mfma_i32_16x16x64_i8 v[50:53], v[168:171], v[184:187], v[50:53]
	v_mfma_i32_16x16x64_i8 v[46:49], v[150:153], v[192:195], v[46:49]
	v_mfma_i32_16x16x64_i8 v[42:45], v[168:171], v[192:195], v[42:45]
	v_mfma_i32_16x16x64_i8 v[38:41], v[150:153], v[202:205], v[38:41]
	v_mfma_i32_16x16x64_i8 v[34:37], v[168:171], v[202:205], v[34:37]
	s_setprio 0
	s_barrier
	s_add_i32 s68, 0, 0x1c000
	s_add_i32 s69, s90, s4
	v_add_u32_e32 v154, s68, v157
	v_lshl_add_u64 v[222:223], v[222:223], 0, s[28:29]
	s_mov_b32 m0, s69
	ds_read_b128 v[206:209], v154
	ds_read_b128 v[210:213], v154 offset:1024
	ds_read_b128 v[214:217], v154 offset:2048
	ds_read_b128 v[218:221], v154 offset:3072
	global_load_lds_dwordx4 v[222:223], off
	v_lshl_add_u64 v[222:223], v[224:225], 0, s[28:29]
	s_add_i32 m0, s69, 0x2000
	s_nop 0
	global_load_lds_dwordx4 v[222:223], off
	s_barrier
	s_waitcnt lgkmcnt(0)
	s_setprio 1
	s_waitcnt lgkmcnt(0)
	v_mfma_i32_16x16x64_i8 v[126:129], v[206:209], v[172:175], v[126:129]
	v_mfma_i32_16x16x64_i8 v[122:125], v[214:217], v[172:175], v[122:125]
	ds_read_b128 v[172:175], v159 offset:49152
	v_mfma_i32_16x16x64_i8 v[118:121], v[206:209], v[180:183], v[118:121]
	v_mfma_i32_16x16x64_i8 v[114:117], v[214:217], v[180:183], v[114:117]
	ds_read_b128 v[180:183], v159 offset:51200
	v_mfma_i32_16x16x64_i8 v[110:113], v[206:209], v[188:191], v[110:113]
	v_mfma_i32_16x16x64_i8 v[106:109], v[214:217], v[188:191], v[106:109]
	ds_read_b128 v[188:191], v159 offset:53248
	v_mfma_i32_16x16x64_i8 v[102:105], v[206:209], v[198:201], v[102:105]
	v_mfma_i32_16x16x64_i8 v[98:101], v[214:217], v[198:201], v[98:101]
	ds_read_b128 v[198:201], v159 offset:55296
	v_mfma_i32_16x16x64_i8 v[126:129], v[210:213], v[176:179], v[126:129]
	v_mfma_i32_16x16x64_i8 v[122:125], v[218:221], v[176:179], v[122:125]
	ds_read_b128 v[176:179], v159 offset:50176
	v_mfma_i32_16x16x64_i8 v[118:121], v[210:213], v[184:187], v[118:121]
	v_mfma_i32_16x16x64_i8 v[114:117], v[218:221], v[184:187], v[114:117]
	ds_read_b128 v[184:187], v159 offset:52224
	v_mfma_i32_16x16x64_i8 v[110:113], v[210:213], v[192:195], v[110:113]
	v_mfma_i32_16x16x64_i8 v[106:109], v[218:221], v[192:195], v[106:109]
	ds_read_b128 v[192:195], v159 offset:54272
	v_mfma_i32_16x16x64_i8 v[102:105], v[210:213], v[202:205], v[102:105]
	v_mfma_i32_16x16x64_i8 v[98:101], v[218:221], v[202:205], v[98:101]
	ds_read_b128 v[202:205], v159 offset:56320
	s_setprio 0
	s_mov_b32 m0, s73
	v_lshl_add_u64 v[222:223], v[226:227], 0, s[28:29]
	s_barrier
	global_load_lds_dwordx4 v[222:223], off
	v_lshl_add_u64 v[222:223], v[228:229], 0, s[28:29]
	s_mov_b32 m0, s74
	s_nop 0
	global_load_lds_dwordx4 v[222:223], off
	s_barrier
	s_waitcnt lgkmcnt(0)
	s_setprio 1
	s_waitcnt lgkmcnt(0)
	v_mfma_i32_16x16x64_i8 v[30:33], v[146:149], v[172:175], v[30:33]
	v_mfma_i32_16x16x64_i8 v[26:29], v[164:167], v[172:175], v[26:29]
	v_mfma_i32_16x16x64_i8 v[22:25], v[146:149], v[180:183], v[22:25]
	v_mfma_i32_16x16x64_i8 v[18:21], v[164:167], v[180:183], v[18:21]
	v_mfma_i32_16x16x64_i8 v[14:17], v[146:149], v[188:191], v[14:17]
	v_mfma_i32_16x16x64_i8 v[10:13], v[164:167], v[188:191], v[10:13]
	v_mfma_i32_16x16x64_i8 v[6:9], v[146:149], v[198:201], v[6:9]
	v_mfma_i32_16x16x64_i8 v[2:5], v[164:167], v[198:201], v[2:5]
	v_mfma_i32_16x16x64_i8 v[30:33], v[150:153], v[176:179], v[30:33]
	v_mfma_i32_16x16x64_i8 v[26:29], v[168:171], v[176:179], v[26:29]
	v_mfma_i32_16x16x64_i8 v[22:25], v[150:153], v[184:187], v[22:25]
	v_mfma_i32_16x16x64_i8 v[18:21], v[168:171], v[184:187], v[18:21]
	v_mfma_i32_16x16x64_i8 v[14:17], v[150:153], v[192:195], v[14:17]
	v_mfma_i32_16x16x64_i8 v[10:13], v[168:171], v[192:195], v[10:13]
	v_mfma_i32_16x16x64_i8 v[6:9], v[150:153], v[202:205], v[6:9]
	v_mfma_i32_16x16x64_i8 v[2:5], v[168:171], v[202:205], v[2:5]
	s_setprio 0
	s_barrier
	s_add_u32 s66, s66, 0x40080
	s_addc_u32 s67, s67, 0
	s_add_i32 s68, s68, s4
	v_lshl_add_u64 v[146:147], s[66:67], 0, v[134:135]
	s_mov_b32 m0, s68
	s_nop 0
	global_load_lds_dwordx4 v[146:147], off
	v_lshl_add_u64 v[146:147], s[66:67], 0, v[130:131]
	s_add_i32 m0, s68, 0x2000
	s_nop 0
	global_load_lds_dwordx4 v[146:147], off
	s_waitcnt vmcnt(6)
	s_barrier
	s_setprio 1
	v_mfma_i32_16x16x64_i8 v[94:97], v[206:209], v[172:175], v[94:97]
	v_mfma_i32_16x16x64_i8 v[90:93], v[214:217], v[172:175], v[90:93]
	v_mfma_i32_16x16x64_i8 v[86:89], v[206:209], v[180:183], v[86:89]
	v_mfma_i32_16x16x64_i8 v[82:85], v[214:217], v[180:183], v[82:85]
	v_mfma_i32_16x16x64_i8 v[78:81], v[206:209], v[188:191], v[78:81]
	v_mfma_i32_16x16x64_i8 v[74:77], v[214:217], v[188:191], v[74:77]
	v_mfma_i32_16x16x64_i8 v[70:73], v[206:209], v[198:201], v[70:73]
	v_mfma_i32_16x16x64_i8 v[66:69], v[214:217], v[198:201], v[66:69]
	v_mfma_i32_16x16x64_i8 v[94:97], v[210:213], v[176:179], v[94:97]
	v_mfma_i32_16x16x64_i8 v[90:93], v[218:221], v[176:179], v[90:93]
	v_mfma_i32_16x16x64_i8 v[86:89], v[210:213], v[184:187], v[86:89]
	v_mfma_i32_16x16x64_i8 v[82:85], v[218:221], v[184:187], v[82:85]
	v_mfma_i32_16x16x64_i8 v[78:81], v[210:213], v[192:195], v[78:81]
	v_mfma_i32_16x16x64_i8 v[74:77], v[218:221], v[192:195], v[74:77]
	v_mfma_i32_16x16x64_i8 v[70:73], v[210:213], v[202:205], v[70:73]
	v_mfma_i32_16x16x64_i8 v[66:69], v[218:221], v[202:205], v[66:69]
	s_setprio 0
	s_add_u32 s10, s10, 0x100
	s_addc_u32 s11, s11, 0
	s_add_u32 s87, s87, 0x100
	s_addc_u32 s88, s88, 0
	s_cmp_ge_i32 s89, s1
	s_mov_b32 s66, s89
	s_barrier
	s_cbranch_scc0 .LBB0_193
	s_branch .Lmy_pl0_exit
.LBB0_193:
	s_waitcnt vmcnt(0)
	v_add_u32_e32 v154, s77, v157
	ds_read_b128 v[146:149], v154
	ds_read_b128 v[150:153], v154 offset:1024
	ds_read_b128 v[164:167], v154 offset:2048
	ds_read_b128 v[168:171], v154 offset:3072
	s_add_i32 s89, s66, 2
	s_add_u32 s67, s10, 0xfffc0080
	s_addc_u32 s68, s11, -1
	s_cmp_eq_u32 s75, s66
	s_cselect_b32 s66, s86, s87
	s_cselect_b32 s69, s9, s68
	s_cselect_b32 s68, s59, s67
	s_cselect_b32 s67, s61, s88
	v_lshl_add_u64 v[206:207], s[10:11], 0, v[138:139]
	s_add_i32 m0, s52, 0xc000
	ds_read_b128 v[172:175], v159
	ds_read_b128 v[176:179], v159 offset:1024
	ds_read_b128 v[180:183], v159 offset:2048
	ds_read_b128 v[184:187], v159 offset:3072
	ds_read_b128 v[188:191], v159 offset:4096
	ds_read_b128 v[192:195], v159 offset:5120
	ds_read_b128 v[198:201], v159 offset:6144
	ds_read_b128 v[202:205], v159 offset:7168
	global_load_lds_dwordx4 v[206:207], off
	v_lshl_add_u64 v[206:207], s[10:11], 0, v[140:141]
	s_add_i32 m0, s52, 0xe000
	s_nop 0
	global_load_lds_dwordx4 v[206:207], off
	s_waitcnt lgkmcnt(8)
	s_barrier
	s_waitcnt lgkmcnt(0)
	s_setprio 1
	s_waitcnt lgkmcnt(0)
	v_mfma_i32_16x16x64_i8 v[62:65], v[146:149], v[172:175], v[62:65]
	v_add_u32_e32 v154, s78, v157
	ds_read_b128 v[218:221], v154 offset:3072
	ds_read_b128 v[214:217], v154 offset:2048
	ds_read_b128 v[210:213], v154 offset:1024
	ds_read_b128 v[206:209], v154
	v_mfma_i32_16x16x64_i8 v[58:61], v[164:167], v[172:175], v[58:61]
	v_mfma_i32_16x16x64_i8 v[54:57], v[146:149], v[180:183], v[54:57]
	v_mfma_i32_16x16x64_i8 v[50:53], v[164:167], v[180:183], v[50:53]
	v_mfma_i32_16x16x64_i8 v[46:49], v[146:149], v[188:191], v[46:49]
	v_mfma_i32_16x16x64_i8 v[42:45], v[164:167], v[188:191], v[42:45]
	v_mfma_i32_16x16x64_i8 v[38:41], v[146:149], v[198:201], v[38:41]
	v_mfma_i32_16x16x64_i8 v[34:37], v[164:167], v[198:201], v[34:37]
	v_mfma_i32_16x16x64_i8 v[62:65], v[150:153], v[176:179], v[62:65]
	v_mfma_i32_16x16x64_i8 v[58:61], v[168:171], v[176:179], v[58:61]
	v_mfma_i32_16x16x64_i8 v[54:57], v[150:153], v[184:187], v[54:57]
	v_mfma_i32_16x16x64_i8 v[50:53], v[168:171], v[184:187], v[50:53]
	v_mfma_i32_16x16x64_i8 v[46:49], v[150:153], v[192:195], v[46:49]
	v_mfma_i32_16x16x64_i8 v[42:45], v[168:171], v[192:195], v[42:45]
	v_mfma_i32_16x16x64_i8 v[38:41], v[150:153], v[202:205], v[38:41]
	v_mfma_i32_16x16x64_i8 v[34:37], v[168:171], v[202:205], v[34:37]
	s_setprio 0
	s_barrier
	s_add_i32 s90, s77, s4
	v_lshl_add_u64 v[222:223], s[66:67], 0, v[134:135]
	s_mov_b32 m0, s90
	global_load_lds_dwordx4 v[222:223], off
	v_lshl_add_u64 v[224:225], s[66:67], 0, v[130:131]
	s_add_i32 m0, s90, 0x2000
	s_nop 0
	global_load_lds_dwordx4 v[224:225], off
	s_barrier
	s_waitcnt lgkmcnt(0)
	s_setprio 1
	s_waitcnt lgkmcnt(0)
	v_mfma_i32_16x16x64_i8 v[126:129], v[206:209], v[172:175], v[126:129]
	v_mfma_i32_16x16x64_i8 v[122:125], v[214:217], v[172:175], v[122:125]
	ds_read_b128 v[172:175], v159 offset:16384
	v_mfma_i32_16x16x64_i8 v[118:121], v[206:209], v[180:183], v[118:121]
	v_mfma_i32_16x16x64_i8 v[114:117], v[214:217], v[180:183], v[114:117]
	ds_read_b128 v[180:183], v159 offset:18432
	v_mfma_i32_16x16x64_i8 v[110:113], v[206:209], v[188:191], v[110:113]
	v_mfma_i32_16x16x64_i8 v[106:109], v[214:217], v[188:191], v[106:109]
	ds_read_b128 v[188:191], v159 offset:20480
	v_mfma_i32_16x16x64_i8 v[102:105], v[206:209], v[198:201], v[102:105]
	v_mfma_i32_16x16x64_i8 v[98:101], v[214:217], v[198:201], v[98:101]
	ds_read_b128 v[198:201], v159 offset:22528
	v_mfma_i32_16x16x64_i8 v[126:129], v[210:213], v[176:179], v[126:129]
	v_mfma_i32_16x16x64_i8 v[122:125], v[218:221], v[176:179], v[122:125]
	ds_read_b128 v[176:179], v159 offset:17408
	v_mfma_i32_16x16x64_i8 v[118:121], v[210:213], v[184:187], v[118:121]
	v_mfma_i32_16x16x64_i8 v[114:117], v[218:221], v[184:187], v[114:117]
	ds_read_b128 v[184:187], v159 offset:19456
	v_mfma_i32_16x16x64_i8 v[110:113], v[210:213], v[192:195], v[110:113]
	v_mfma_i32_16x16x64_i8 v[106:109], v[218:221], v[192:195], v[106:109]
	ds_read_b128 v[192:195], v159 offset:21504
	v_mfma_i32_16x16x64_i8 v[102:105], v[210:213], v[202:205], v[102:105]
	v_mfma_i32_16x16x64_i8 v[98:101], v[218:221], v[202:205], v[98:101]
	ds_read_b128 v[202:205], v159 offset:23552
	s_setprio 0
	s_mov_b32 m0, s52
	v_lshl_add_u64 v[226:227], s[68:69], 0, v[136:137]
	s_barrier
	global_load_lds_dwordx4 v[226:227], off
	v_lshl_add_u64 v[228:229], s[68:69], 0, v[132:133]
	s_mov_b32 m0, s53
	s_nop 0
	global_load_lds_dwordx4 v[228:229], off
	s_barrier
	s_waitcnt lgkmcnt(0)
	s_setprio 1
	s_waitcnt lgkmcnt(0)
	v_mfma_i32_16x16x64_i8 v[30:33], v[146:149], v[172:175], v[30:33]
	v_mfma_i32_16x16x64_i8 v[26:29], v[164:167], v[172:175], v[26:29]
	v_mfma_i32_16x16x64_i8 v[22:25], v[146:149], v[180:183], v[22:25]
	v_mfma_i32_16x16x64_i8 v[18:21], v[164:167], v[180:183], v[18:21]
	v_mfma_i32_16x16x64_i8 v[14:17], v[146:149], v[188:191], v[14:17]
	v_mfma_i32_16x16x64_i8 v[10:13], v[164:167], v[188:191], v[10:13]
	v_mfma_i32_16x16x64_i8 v[6:9], v[146:149], v[198:201], v[6:9]
	v_mfma_i32_16x16x64_i8 v[2:5], v[164:167], v[198:201], v[2:5]
	v_mfma_i32_16x16x64_i8 v[30:33], v[150:153], v[176:179], v[30:33]
	v_mfma_i32_16x16x64_i8 v[26:29], v[168:171], v[176:179], v[26:29]
	v_mfma_i32_16x16x64_i8 v[22:25], v[150:153], v[184:187], v[22:25]
	v_mfma_i32_16x16x64_i8 v[18:21], v[168:171], v[184:187], v[18:21]
	v_mfma_i32_16x16x64_i8 v[14:17], v[150:153], v[192:195], v[14:17]
	v_mfma_i32_16x16x64_i8 v[10:13], v[168:171], v[192:195], v[10:13]
	v_mfma_i32_16x16x64_i8 v[6:9], v[150:153], v[202:205], v[6:9]
	v_mfma_i32_16x16x64_i8 v[2:5], v[168:171], v[202:205], v[2:5]
	s_setprio 0
	s_barrier
	s_add_u32 s90, s66, 0x40000
	s_addc_u32 s91, s67, 0
	s_add_i32 s92, s78, s4
	v_lshl_add_u64 v[146:147], s[90:91], 0, v[134:135]
	s_mov_b32 m0, s92
	s_nop 0
	global_load_lds_dwordx4 v[146:147], off
	v_lshl_add_u64 v[146:147], s[90:91], 0, v[130:131]
	s_add_i32 m0, s92, 0x2000
	s_nop 0
	global_load_lds_dwordx4 v[146:147], off
	s_waitcnt vmcnt(6)
	s_barrier
	s_setprio 1
	v_mfma_i32_16x16x64_i8 v[94:97], v[206:209], v[172:175], v[94:97]
	v_mfma_i32_16x16x64_i8 v[90:93], v[214:217], v[172:175], v[90:93]
	ds_read_b128 v[172:175], v159 offset:32768
	v_mfma_i32_16x16x64_i8 v[86:89], v[206:209], v[180:183], v[86:89]
	v_mfma_i32_16x16x64_i8 v[82:85], v[214:217], v[180:183], v[82:85]
	ds_read_b128 v[180:183], v159 offset:34816
	v_mfma_i32_16x16x64_i8 v[78:81], v[206:209], v[188:191], v[78:81]
	v_mfma_i32_16x16x64_i8 v[74:77], v[214:217], v[188:191], v[74:77]
	ds_read_b128 v[188:191], v159 offset:36864
	v_mfma_i32_16x16x64_i8 v[70:73], v[206:209], v[198:201], v[70:73]
	v_mfma_i32_16x16x64_i8 v[66:69], v[214:217], v[198:201], v[66:69]
	ds_read_b128 v[198:201], v159 offset:38912
	v_mfma_i32_16x16x64_i8 v[94:97], v[210:213], v[176:179], v[94:97]
	v_mfma_i32_16x16x64_i8 v[90:93], v[218:221], v[176:179], v[90:93]
	ds_read_b128 v[176:179], v159 offset:33792
	v_mfma_i32_16x16x64_i8 v[86:89], v[210:213], v[184:187], v[86:89]
	v_mfma_i32_16x16x64_i8 v[82:85], v[218:221], v[184:187], v[82:85]
	ds_read_b128 v[184:187], v159 offset:35840
	v_mfma_i32_16x16x64_i8 v[78:81], v[210:213], v[192:195], v[78:81]
	v_mfma_i32_16x16x64_i8 v[74:77], v[218:221], v[192:195], v[74:77]
	ds_read_b128 v[192:195], v159 offset:37888
	v_mfma_i32_16x16x64_i8 v[70:73], v[210:213], v[202:205], v[70:73]
	v_mfma_i32_16x16x64_i8 v[66:69], v[218:221], v[202:205], v[66:69]
	ds_read_b128 v[202:205], v159 offset:39936
	s_setprio 0
	s_add_i32 s90, 0, 0x18000
	v_add_u32_e32 v154, s90, v157
	s_barrier
	ds_read_b128 v[146:149], v154
	ds_read_b128 v[150:153], v154 offset:1024
	ds_read_b128 v[164:167], v154 offset:2048
	ds_read_b128 v[168:171], v154 offset:3072
	s_add_u32 s68, s68, 0x40000
	s_addc_u32 s69, s69, 0
	s_mov_b32 m0, s54
	v_lshl_add_u64 v[206:207], s[68:69], 0, v[136:137]
	global_load_lds_dwordx4 v[206:207], off
	v_lshl_add_u64 v[206:207], s[68:69], 0, v[132:133]
	s_mov_b32 m0, s55
	s_nop 0
	global_load_lds_dwordx4 v[206:207], off
	s_waitcnt lgkmcnt(8)
	s_barrier
	s_waitcnt lgkmcnt(0)
	s_setprio 1
	s_waitcnt lgkmcnt(0)
	v_mfma_i32_16x16x64_i8 v[62:65], v[146:149], v[172:175], v[62:65]
	v_mfma_i32_16x16x64_i8 v[58:61], v[164:167], v[172:175], v[58:61]
	v_mfma_i32_16x16x64_i8 v[54:57], v[146:149], v[180:183], v[54:57]
	v_mfma_i32_16x16x64_i8 v[50:53], v[164:167], v[180:183], v[50:53]
	v_mfma_i32_16x16x64_i8 v[46:49], v[146:149], v[188:191], v[46:49]
	v_mfma_i32_16x16x64_i8 v[42:45], v[164:167], v[188:191], v[42:45]
	v_mfma_i32_16x16x64_i8 v[38:41], v[146:149], v[198:201], v[38:41]
	v_mfma_i32_16x16x64_i8 v[34:37], v[164:167], v[198:201], v[34:37]
	v_mfma_i32_16x16x64_i8 v[62:65], v[150:153], v[176:179], v[62:65]
	v_mfma_i32_16x16x64_i8 v[58:61], v[168:171], v[176:179], v[58:61]
	v_mfma_i32_16x16x64_i8 v[54:57], v[150:153], v[184:187], v[54:57]
	v_mfma_i32_16x16x64_i8 v[50:53], v[168:171], v[184:187], v[50:53]
	v_mfma_i32_16x16x64_i8 v[46:49], v[150:153], v[192:195], v[46:49]
	v_mfma_i32_16x16x64_i8 v[42:45], v[168:171], v[192:195], v[42:45]
	v_mfma_i32_16x16x64_i8 v[38:41], v[150:153], v[202:205], v[38:41]
	v_mfma_i32_16x16x64_i8 v[34:37], v[168:171], v[202:205], v[34:37]
	s_setprio 0
	s_barrier
	s_add_i32 s68, 0, 0x1c000
	s_add_i32 s69, s90, s4
	v_add_u32_e32 v154, s68, v157
	v_lshl_add_u64 v[222:223], v[222:223], 0, s[28:29]
	s_mov_b32 m0, s69
	ds_read_b128 v[206:209], v154
	ds_read_b128 v[210:213], v154 offset:1024
	ds_read_b128 v[214:217], v154 offset:2048
	ds_read_b128 v[218:221], v154 offset:3072
	global_load_lds_dwordx4 v[222:223], off
	v_lshl_add_u64 v[222:223], v[224:225], 0, s[28:29]
	s_add_i32 m0, s69, 0x2000
	s_nop 0
	global_load_lds_dwordx4 v[222:223], off
	s_barrier
	s_waitcnt lgkmcnt(0)
	s_setprio 1
	s_waitcnt lgkmcnt(0)
	v_mfma_i32_16x16x64_i8 v[126:129], v[206:209], v[172:175], v[126:129]
	v_mfma_i32_16x16x64_i8 v[122:125], v[214:217], v[172:175], v[122:125]
	ds_read_b128 v[172:175], v159 offset:49152
	v_mfma_i32_16x16x64_i8 v[118:121], v[206:209], v[180:183], v[118:121]
	v_mfma_i32_16x16x64_i8 v[114:117], v[214:217], v[180:183], v[114:117]
	ds_read_b128 v[180:183], v159 offset:51200
	v_mfma_i32_16x16x64_i8 v[110:113], v[206:209], v[188:191], v[110:113]
	v_mfma_i32_16x16x64_i8 v[106:109], v[214:217], v[188:191], v[106:109]
	ds_read_b128 v[188:191], v159 offset:53248
	v_mfma_i32_16x16x64_i8 v[102:105], v[206:209], v[198:201], v[102:105]
	v_mfma_i32_16x16x64_i8 v[98:101], v[214:217], v[198:201], v[98:101]
	ds_read_b128 v[198:201], v159 offset:55296
	v_mfma_i32_16x16x64_i8 v[126:129], v[210:213], v[176:179], v[126:129]
	v_mfma_i32_16x16x64_i8 v[122:125], v[218:221], v[176:179], v[122:125]
	ds_read_b128 v[176:179], v159 offset:50176
	v_mfma_i32_16x16x64_i8 v[118:121], v[210:213], v[184:187], v[118:121]
	v_mfma_i32_16x16x64_i8 v[114:117], v[218:221], v[184:187], v[114:117]
	ds_read_b128 v[184:187], v159 offset:52224
	v_mfma_i32_16x16x64_i8 v[110:113], v[210:213], v[192:195], v[110:113]
	v_mfma_i32_16x16x64_i8 v[106:109], v[218:221], v[192:195], v[106:109]
	ds_read_b128 v[192:195], v159 offset:54272
	v_mfma_i32_16x16x64_i8 v[102:105], v[210:213], v[202:205], v[102:105]
	v_mfma_i32_16x16x64_i8 v[98:101], v[218:221], v[202:205], v[98:101]
	ds_read_b128 v[202:205], v159 offset:56320
	s_setprio 0
	s_mov_b32 m0, s73
	v_lshl_add_u64 v[222:223], v[226:227], 0, s[28:29]
	s_barrier
	global_load_lds_dwordx4 v[222:223], off
	v_lshl_add_u64 v[222:223], v[228:229], 0, s[28:29]
	s_mov_b32 m0, s74
	s_nop 0
	global_load_lds_dwordx4 v[222:223], off
	s_barrier
	s_waitcnt lgkmcnt(0)
	s_setprio 1
	s_waitcnt lgkmcnt(0)
	v_mfma_i32_16x16x64_i8 v[30:33], v[146:149], v[172:175], v[30:33]
	v_mfma_i32_16x16x64_i8 v[26:29], v[164:167], v[172:175], v[26:29]
	v_mfma_i32_16x16x64_i8 v[22:25], v[146:149], v[180:183], v[22:25]
	v_mfma_i32_16x16x64_i8 v[18:21], v[164:167], v[180:183], v[18:21]
	v_mfma_i32_16x16x64_i8 v[14:17], v[146:149], v[188:191], v[14:17]
	v_mfma_i32_16x16x64_i8 v[10:13], v[164:167], v[188:191], v[10:13]
	v_mfma_i32_16x16x64_i8 v[6:9], v[146:149], v[198:201], v[6:9]
	v_mfma_i32_16x16x64_i8 v[2:5], v[164:167], v[198:201], v[2:5]
	v_mfma_i32_16x16x64_i8 v[30:33], v[150:153], v[176:179], v[30:33]
	v_mfma_i32_16x16x64_i8 v[26:29], v[168:171], v[176:179], v[26:29]
	v_mfma_i32_16x16x64_i8 v[22:25], v[150:153], v[184:187], v[22:25]
	v_mfma_i32_16x16x64_i8 v[18:21], v[168:171], v[184:187], v[18:21]
	v_mfma_i32_16x16x64_i8 v[14:17], v[150:153], v[192:195], v[14:17]
	v_mfma_i32_16x16x64_i8 v[10:13], v[168:171], v[192:195], v[10:13]
	v_mfma_i32_16x16x64_i8 v[6:9], v[150:153], v[202:205], v[6:9]
	v_mfma_i32_16x16x64_i8 v[2:5], v[168:171], v[202:205], v[2:5]
	s_setprio 0
	s_barrier
	s_add_u32 s66, s66, 0x40080
	s_addc_u32 s67, s67, 0
	s_add_i32 s68, s68, s4
	v_lshl_add_u64 v[146:147], s[66:67], 0, v[134:135]
	s_mov_b32 m0, s68
	s_nop 0
	global_load_lds_dwordx4 v[146:147], off
	v_lshl_add_u64 v[146:147], s[66:67], 0, v[130:131]
	s_add_i32 m0, s68, 0x2000
	s_nop 0
	global_load_lds_dwordx4 v[146:147], off
	s_waitcnt vmcnt(6)
	s_barrier
	s_setprio 1
	v_mfma_i32_16x16x64_i8 v[94:97], v[206:209], v[172:175], v[94:97]
	v_mfma_i32_16x16x64_i8 v[90:93], v[214:217], v[172:175], v[90:93]
	v_mfma_i32_16x16x64_i8 v[86:89], v[206:209], v[180:183], v[86:89]
	v_mfma_i32_16x16x64_i8 v[82:85], v[214:217], v[180:183], v[82:85]
	v_mfma_i32_16x16x64_i8 v[78:81], v[206:209], v[188:191], v[78:81]
	v_mfma_i32_16x16x64_i8 v[74:77], v[214:217], v[188:191], v[74:77]
	v_mfma_i32_16x16x64_i8 v[70:73], v[206:209], v[198:201], v[70:73]
	v_mfma_i32_16x16x64_i8 v[66:69], v[214:217], v[198:201], v[66:69]
	v_mfma_i32_16x16x64_i8 v[94:97], v[210:213], v[176:179], v[94:97]
	v_mfma_i32_16x16x64_i8 v[90:93], v[218:221], v[176:179], v[90:93]
	v_mfma_i32_16x16x64_i8 v[86:89], v[210:213], v[184:187], v[86:89]
	v_mfma_i32_16x16x64_i8 v[82:85], v[218:221], v[184:187], v[82:85]
	v_mfma_i32_16x16x64_i8 v[78:81], v[210:213], v[192:195], v[78:81]
	v_mfma_i32_16x16x64_i8 v[74:77], v[218:221], v[192:195], v[74:77]
	v_mfma_i32_16x16x64_i8 v[70:73], v[210:213], v[202:205], v[70:73]
	v_mfma_i32_16x16x64_i8 v[66:69], v[218:221], v[202:205], v[66:69]
	s_setprio 0
	s_add_u32 s10, s10, 0x100
	s_addc_u32 s11, s11, 0
	s_add_u32 s87, s87, 0x100
	s_addc_u32 s88, s88, 0
	s_cmp_ge_i32 s89, s1
	s_mov_b32 s66, s89
	s_barrier
	s_cbranch_scc0 .LBB0_193

.LBB0_962:
	s_ashr_i32 s27, s26, 31
	s_lshl_b64 s[28:29], s[26:27], 20
	s_add_u32 s28, s10, s28
	s_addc_u32 s29, s11, s29
	s_ashr_i32 s25, s24, 31
	s_lshl_b64 s[30:31], s[24:25], 20
	s_add_u32 s30, s14, s30
	v_cmp_lt_i64_e64 s[8:9], s[8:9], v[158:159]
	s_addc_u32 s31, s15, s31
	s_andn2_b64 vcc, exec, s[20:21]
	s_cbranch_vccnz .LBB0_954
	s_and_b64 s[8:9], s[8:9], exec
	s_cselect_b32 s25, s29, s39
	s_cselect_b32 s27, s28, s38
	s_cselect_b32 s51, s31, s37
	s_cselect_b32 s52, s30, s36
	s_add_u32 s8, s38, 0x80080
	s_addc_u32 s9, s39, 0
	s_add_u32 s53, s36, 0x100
	v_mov_b32_e32 v2, 0
	s_addc_u32 s54, s37, 0
	s_mov_b32 s36, 0
	ds_read_b128 v[130:133], v172
	ds_read_b128 v[134:137], v172 offset:1024
	ds_read_b128 v[138:141], v172 offset:2048
	ds_read_b128 v[142:145], v172 offset:3072
	s_add_i32 s55, s36, 2
	s_add_u32 s37, s8, 0xfff80080
	s_addc_u32 s38, s9, -1
	s_cmp_eq_u32 s46, s36
	s_cselect_b32 s36, s52, s53
	s_cselect_b32 s39, s25, s38
	s_cselect_b32 s38, s27, s37
	s_cselect_b32 s37, s51, s54
	v_lshl_add_u64 v[200:201], s[8:9], 0, v[154:155]
	s_add_i32 m0, s23, 0xc000
	ds_read_b128 v[162:165], v173
	ds_read_b128 v[166:169], v173 offset:1024
	ds_read_b128 v[176:179], v173 offset:2048
	ds_read_b128 v[180:183], v173 offset:3072
	ds_read_b128 v[184:187], v173 offset:4096
	ds_read_b128 v[188:191], v173 offset:5120
	ds_read_b128 v[192:195], v173 offset:6144
	ds_read_b128 v[196:199], v173 offset:7168
	global_load_lds_dwordx4 v[200:201], off
	v_lshl_add_u64 v[200:201], s[8:9], 0, v[156:157]
	s_add_i32 m0, s23, 0xe000
	s_nop 0
	global_load_lds_dwordx4 v[200:201], off
	s_waitcnt lgkmcnt(8)
	s_barrier
	s_waitcnt lgkmcnt(0)
	s_setprio 1
	s_waitcnt lgkmcnt(0)
	v_mfma_f32_16x16x32_bf16 v[126:129], v[130:133], v[162:165], 0
	ds_read_b128 v[214:217], v174 offset:3072
	ds_read_b128 v[208:211], v174 offset:2048
	ds_read_b128 v[204:207], v174 offset:1024
	ds_read_b128 v[200:203], v174
	v_mfma_f32_16x16x32_bf16 v[122:125], v[138:141], v[162:165], 0
	v_mfma_f32_16x16x32_bf16 v[110:113], v[130:133], v[176:179], 0
	v_mfma_f32_16x16x32_bf16 v[106:109], v[138:141], v[176:179], 0
	v_mfma_f32_16x16x32_bf16 v[94:97], v[130:133], v[184:187], 0
	v_mfma_f32_16x16x32_bf16 v[90:93], v[138:141], v[184:187], 0
	v_mfma_f32_16x16x32_bf16 v[78:81], v[130:133], v[192:195], 0
	v_mfma_f32_16x16x32_bf16 v[74:77], v[138:141], v[192:195], 0
	v_mfma_f32_16x16x32_bf16 v[126:129], v[134:137], v[166:169], v[126:129]
	v_mfma_f32_16x16x32_bf16 v[122:125], v[142:145], v[166:169], v[122:125]
	v_mfma_f32_16x16x32_bf16 v[110:113], v[134:137], v[180:183], v[110:113]
	v_mfma_f32_16x16x32_bf16 v[106:109], v[142:145], v[180:183], v[106:109]
	v_mfma_f32_16x16x32_bf16 v[94:97], v[134:137], v[188:191], v[94:97]
	v_mfma_f32_16x16x32_bf16 v[90:93], v[142:145], v[188:191], v[90:93]
	v_mfma_f32_16x16x32_bf16 v[78:81], v[134:137], v[196:199], v[78:81]
	v_mfma_f32_16x16x32_bf16 v[74:77], v[142:145], v[196:199], v[74:77]
	s_setprio 0
	s_barrier
	s_add_i32 s56, s48, s5
	v_lshl_add_u64 v[218:219], s[36:37], 0, v[148:149]
	s_mov_b32 m0, s56
	global_load_lds_dwordx4 v[218:219], off
	v_lshl_add_u64 v[220:221], s[36:37], 0, v[152:153]
	s_add_i32 m0, s56, 0x2000
	s_nop 0
	global_load_lds_dwordx4 v[220:221], off
	s_barrier
	s_waitcnt lgkmcnt(0)
	s_setprio 1
	s_waitcnt lgkmcnt(0)
	v_mfma_f32_16x16x32_bf16 v[118:121], v[200:203], v[162:165], 0
	v_mfma_f32_16x16x32_bf16 v[114:117], v[208:211], v[162:165], 0
	ds_read_b128 v[162:165], v173 offset:16384
	v_mfma_f32_16x16x32_bf16 v[102:105], v[200:203], v[176:179], 0
	v_mfma_f32_16x16x32_bf16 v[98:101], v[208:211], v[176:179], 0
	ds_read_b128 v[176:179], v173 offset:18432
	v_mfma_f32_16x16x32_bf16 v[86:89], v[200:203], v[184:187], 0
	v_mfma_f32_16x16x32_bf16 v[82:85], v[208:211], v[184:187], 0
	ds_read_b128 v[184:187], v173 offset:20480
	v_mfma_f32_16x16x32_bf16 v[70:73], v[200:203], v[192:195], 0
	v_mfma_f32_16x16x32_bf16 v[66:69], v[208:211], v[192:195], 0
	ds_read_b128 v[192:195], v173 offset:22528
	v_mfma_f32_16x16x32_bf16 v[118:121], v[204:207], v[166:169], v[118:121]
	v_mfma_f32_16x16x32_bf16 v[114:117], v[214:217], v[166:169], v[114:117]
	ds_read_b128 v[166:169], v173 offset:17408
	v_mfma_f32_16x16x32_bf16 v[102:105], v[204:207], v[180:183], v[102:105]
	v_mfma_f32_16x16x32_bf16 v[98:101], v[214:217], v[180:183], v[98:101]
	ds_read_b128 v[180:183], v173 offset:19456
	v_mfma_f32_16x16x32_bf16 v[86:89], v[204:207], v[188:191], v[86:89]
	v_mfma_f32_16x16x32_bf16 v[82:85], v[214:217], v[188:191], v[82:85]
	ds_read_b128 v[188:191], v173 offset:21504
	v_mfma_f32_16x16x32_bf16 v[70:73], v[204:207], v[196:199], v[70:73]
	v_mfma_f32_16x16x32_bf16 v[66:69], v[214:217], v[196:199], v[66:69]
	ds_read_b128 v[196:199], v173 offset:23552
	s_setprio 0
	s_mov_b32 m0, s23
	v_lshl_add_u64 v[222:223], s[38:39], 0, v[146:147]
	s_barrier
	global_load_lds_dwordx4 v[222:223], off
	v_lshl_add_u64 v[224:225], s[38:39], 0, v[150:151]
	s_mov_b32 m0, s33
	s_nop 0
	global_load_lds_dwordx4 v[224:225], off
	s_barrier
	s_waitcnt lgkmcnt(0)
	s_setprio 1
	s_waitcnt lgkmcnt(0)
	v_mfma_f32_16x16x32_bf16 v[62:65], v[130:133], v[162:165], 0
	v_mfma_f32_16x16x32_bf16 v[58:61], v[138:141], v[162:165], 0
	v_mfma_f32_16x16x32_bf16 v[46:49], v[130:133], v[176:179], 0
	v_mfma_f32_16x16x32_bf16 v[42:45], v[138:141], v[176:179], 0
	v_mfma_f32_16x16x32_bf16 v[30:33], v[130:133], v[184:187], 0
	v_mfma_f32_16x16x32_bf16 v[26:29], v[138:141], v[184:187], 0
	v_mfma_f32_16x16x32_bf16 v[14:17], v[130:133], v[192:195], 0
	v_mfma_f32_16x16x32_bf16 v[10:13], v[138:141], v[192:195], 0
	v_mfma_f32_16x16x32_bf16 v[62:65], v[134:137], v[166:169], v[62:65]
	v_mfma_f32_16x16x32_bf16 v[58:61], v[142:145], v[166:169], v[58:61]
	v_mfma_f32_16x16x32_bf16 v[46:49], v[134:137], v[180:183], v[46:49]
	v_mfma_f32_16x16x32_bf16 v[42:45], v[142:145], v[180:183], v[42:45]
	v_mfma_f32_16x16x32_bf16 v[30:33], v[134:137], v[188:191], v[30:33]
	v_mfma_f32_16x16x32_bf16 v[26:29], v[142:145], v[188:191], v[26:29]
	v_mfma_f32_16x16x32_bf16 v[14:17], v[134:137], v[196:199], v[14:17]
	v_mfma_f32_16x16x32_bf16 v[10:13], v[142:145], v[196:199], v[10:13]
	s_setprio 0
	s_barrier
	s_add_u32 s56, s36, 0x80000
	s_addc_u32 s57, s37, 0
	s_add_i32 s58, s49, s5
	v_lshl_add_u64 v[130:131], s[56:57], 0, v[148:149]
	s_mov_b32 m0, s58
	s_nop 0
	global_load_lds_dwordx4 v[130:131], off
	v_lshl_add_u64 v[130:131], s[56:57], 0, v[152:153]
	s_add_i32 m0, s58, 0x2000
	s_nop 0
	global_load_lds_dwordx4 v[130:131], off
	s_waitcnt vmcnt(6)
	s_barrier
	s_setprio 1
	v_mfma_f32_16x16x32_bf16 v[54:57], v[200:203], v[162:165], 0
	v_mfma_f32_16x16x32_bf16 v[50:53], v[208:211], v[162:165], 0
	ds_read_b128 v[162:165], v173 offset:32768
	v_mfma_f32_16x16x32_bf16 v[38:41], v[200:203], v[176:179], 0
	v_mfma_f32_16x16x32_bf16 v[34:37], v[208:211], v[176:179], 0
	ds_read_b128 v[176:179], v173 offset:34816
	v_mfma_f32_16x16x32_bf16 v[22:25], v[200:203], v[184:187], 0
	v_mfma_f32_16x16x32_bf16 v[18:21], v[208:211], v[184:187], 0
	ds_read_b128 v[184:187], v173 offset:36864
	v_mfma_f32_16x16x32_bf16 v[6:9], v[200:203], v[192:195], 0
	v_mfma_f32_16x16x32_bf16 v[2:5], v[208:211], v[192:195], 0
	ds_read_b128 v[192:195], v173 offset:38912
	v_mfma_f32_16x16x32_bf16 v[54:57], v[204:207], v[166:169], v[54:57]
	v_mfma_f32_16x16x32_bf16 v[50:53], v[214:217], v[166:169], v[50:53]
	ds_read_b128 v[166:169], v173 offset:33792
	v_mfma_f32_16x16x32_bf16 v[38:41], v[204:207], v[180:183], v[38:41]
	v_mfma_f32_16x16x32_bf16 v[34:37], v[214:217], v[180:183], v[34:37]
	ds_read_b128 v[180:183], v173 offset:35840
	v_mfma_f32_16x16x32_bf16 v[22:25], v[204:207], v[188:191], v[22:25]
	v_mfma_f32_16x16x32_bf16 v[18:21], v[214:217], v[188:191], v[18:21]
	ds_read_b128 v[188:191], v173 offset:37888
	v_mfma_f32_16x16x32_bf16 v[6:9], v[204:207], v[196:199], v[6:9]
	v_mfma_f32_16x16x32_bf16 v[2:5], v[214:217], v[196:199], v[2:5]
	ds_read_b128 v[196:199], v173 offset:39936
	s_setprio 0
	s_add_i32 s56, 0, 0x18000
	v_add_u32_e32 v142, s56, v171
	s_barrier
	ds_read_b128 v[130:133], v142
	ds_read_b128 v[134:137], v142 offset:1024
	ds_read_b128 v[138:141], v142 offset:2048
	ds_read_b128 v[142:145], v142 offset:3072
	s_add_u32 s38, s38, 0x80000
	s_addc_u32 s39, s39, 0
	s_mov_b32 m0, s35
	v_lshl_add_u64 v[200:201], s[38:39], 0, v[146:147]
	global_load_lds_dwordx4 v[200:201], off
	v_lshl_add_u64 v[200:201], s[38:39], 0, v[150:151]
	s_mov_b32 m0, s40
	s_nop 0
	global_load_lds_dwordx4 v[200:201], off
	s_waitcnt lgkmcnt(8)
	s_barrier
	s_waitcnt lgkmcnt(0)
	s_setprio 1
	s_waitcnt lgkmcnt(0)
	v_mfma_f32_16x16x32_bf16 v[126:129], v[130:133], v[162:165], v[126:129]
	v_mfma_f32_16x16x32_bf16 v[122:125], v[138:141], v[162:165], v[122:125]
	v_mfma_f32_16x16x32_bf16 v[110:113], v[130:133], v[176:179], v[110:113]
	v_mfma_f32_16x16x32_bf16 v[106:109], v[138:141], v[176:179], v[106:109]
	v_mfma_f32_16x16x32_bf16 v[94:97], v[130:133], v[184:187], v[94:97]
	v_mfma_f32_16x16x32_bf16 v[90:93], v[138:141], v[184:187], v[90:93]
	v_mfma_f32_16x16x32_bf16 v[78:81], v[130:133], v[192:195], v[78:81]
	v_mfma_f32_16x16x32_bf16 v[74:77], v[138:141], v[192:195], v[74:77]
	v_mfma_f32_16x16x32_bf16 v[126:129], v[134:137], v[166:169], v[126:129]
	v_mfma_f32_16x16x32_bf16 v[122:125], v[142:145], v[166:169], v[122:125]
	v_mfma_f32_16x16x32_bf16 v[110:113], v[134:137], v[180:183], v[110:113]
	v_mfma_f32_16x16x32_bf16 v[106:109], v[142:145], v[180:183], v[106:109]
	v_mfma_f32_16x16x32_bf16 v[94:97], v[134:137], v[188:191], v[94:97]
	v_mfma_f32_16x16x32_bf16 v[90:93], v[142:145], v[188:191], v[90:93]
	v_mfma_f32_16x16x32_bf16 v[78:81], v[134:137], v[196:199], v[78:81]
	v_mfma_f32_16x16x32_bf16 v[74:77], v[142:145], v[196:199], v[74:77]
	s_setprio 0
	s_barrier
	s_add_i32 s38, 0, 0x1c000
	s_add_i32 s39, s56, s5
	v_add_u32_e32 v175, s38, v171
	v_lshl_add_u64 v[218:219], v[218:219], 0, s[18:19]
	s_mov_b32 m0, s39
	ds_read_b128 v[200:203], v175
	ds_read_b128 v[204:207], v175 offset:1024
	ds_read_b128 v[208:211], v175 offset:2048
	ds_read_b128 v[214:217], v175 offset:3072
	global_load_lds_dwordx4 v[218:219], off
	v_lshl_add_u64 v[218:219], v[220:221], 0, s[18:19]
	s_add_i32 m0, s39, 0x2000
	s_nop 0
	global_load_lds_dwordx4 v[218:219], off
	s_barrier
	s_waitcnt lgkmcnt(0)
	s_setprio 1
	s_waitcnt lgkmcnt(0)
	v_mfma_f32_16x16x32_bf16 v[118:121], v[200:203], v[162:165], v[118:121]
	v_mfma_f32_16x16x32_bf16 v[114:117], v[208:211], v[162:165], v[114:117]
	ds_read_b128 v[162:165], v173 offset:49152
	v_mfma_f32_16x16x32_bf16 v[102:105], v[200:203], v[176:179], v[102:105]
	v_mfma_f32_16x16x32_bf16 v[98:101], v[208:211], v[176:179], v[98:101]
	ds_read_b128 v[176:179], v173 offset:51200
	v_mfma_f32_16x16x32_bf16 v[86:89], v[200:203], v[184:187], v[86:89]
	v_mfma_f32_16x16x32_bf16 v[82:85], v[208:211], v[184:187], v[82:85]
	ds_read_b128 v[184:187], v173 offset:53248
	v_mfma_f32_16x16x32_bf16 v[70:73], v[200:203], v[192:195], v[70:73]
	v_mfma_f32_16x16x32_bf16 v[66:69], v[208:211], v[192:195], v[66:69]
	ds_read_b128 v[192:195], v173 offset:55296
	v_mfma_f32_16x16x32_bf16 v[118:121], v[204:207], v[166:169], v[118:121]
	v_mfma_f32_16x16x32_bf16 v[114:117], v[214:217], v[166:169], v[114:117]
	ds_read_b128 v[166:169], v173 offset:50176
	v_mfma_f32_16x16x32_bf16 v[102:105], v[204:207], v[180:183], v[102:105]
	v_mfma_f32_16x16x32_bf16 v[98:101], v[214:217], v[180:183], v[98:101]
	ds_read_b128 v[180:183], v173 offset:52224
	v_mfma_f32_16x16x32_bf16 v[86:89], v[204:207], v[188:191], v[86:89]
	v_mfma_f32_16x16x32_bf16 v[82:85], v[214:217], v[188:191], v[82:85]
	ds_read_b128 v[188:191], v173 offset:54272
	v_mfma_f32_16x16x32_bf16 v[70:73], v[204:207], v[196:199], v[70:73]
	v_mfma_f32_16x16x32_bf16 v[66:69], v[214:217], v[196:199], v[66:69]
	ds_read_b128 v[196:199], v173 offset:56320
	s_setprio 0
	s_mov_b32 m0, s44
	v_lshl_add_u64 v[218:219], v[222:223], 0, s[18:19]
	s_barrier
	global_load_lds_dwordx4 v[218:219], off
	v_lshl_add_u64 v[218:219], v[224:225], 0, s[18:19]
	s_mov_b32 m0, s45
	s_nop 0
	global_load_lds_dwordx4 v[218:219], off
	s_barrier
	s_waitcnt lgkmcnt(0)
	s_setprio 1
	s_waitcnt lgkmcnt(0)
	v_mfma_f32_16x16x32_bf16 v[62:65], v[130:133], v[162:165], v[62:65]
	v_mfma_f32_16x16x32_bf16 v[58:61], v[138:141], v[162:165], v[58:61]
	v_mfma_f32_16x16x32_bf16 v[46:49], v[130:133], v[176:179], v[46:49]
	v_mfma_f32_16x16x32_bf16 v[42:45], v[138:141], v[176:179], v[42:45]
	v_mfma_f32_16x16x32_bf16 v[30:33], v[130:133], v[184:187], v[30:33]
	v_mfma_f32_16x16x32_bf16 v[26:29], v[138:141], v[184:187], v[26:29]
	v_mfma_f32_16x16x32_bf16 v[14:17], v[130:133], v[192:195], v[14:17]
	v_mfma_f32_16x16x32_bf16 v[10:13], v[138:141], v[192:195], v[10:13]
	v_mfma_f32_16x16x32_bf16 v[62:65], v[134:137], v[166:169], v[62:65]
	v_mfma_f32_16x16x32_bf16 v[58:61], v[142:145], v[166:169], v[58:61]
	v_mfma_f32_16x16x32_bf16 v[46:49], v[134:137], v[180:183], v[46:49]
	v_mfma_f32_16x16x32_bf16 v[42:45], v[142:145], v[180:183], v[42:45]
	v_mfma_f32_16x16x32_bf16 v[30:33], v[134:137], v[188:191], v[30:33]
	v_mfma_f32_16x16x32_bf16 v[26:29], v[142:145], v[188:191], v[26:29]
	v_mfma_f32_16x16x32_bf16 v[14:17], v[134:137], v[196:199], v[14:17]
	v_mfma_f32_16x16x32_bf16 v[10:13], v[142:145], v[196:199], v[10:13]
	s_setprio 0
	s_barrier
	s_add_u32 s36, s36, 0x80080
	s_addc_u32 s37, s37, 0
	s_add_i32 s38, s38, s5
	v_lshl_add_u64 v[130:131], s[36:37], 0, v[148:149]
	s_mov_b32 m0, s38
	s_nop 0
	global_load_lds_dwordx4 v[130:131], off
	v_lshl_add_u64 v[130:131], s[36:37], 0, v[152:153]
	s_add_i32 m0, s38, 0x2000
	s_nop 0
	global_load_lds_dwordx4 v[130:131], off
	s_waitcnt vmcnt(6)
	s_barrier
	s_setprio 1
	v_mfma_f32_16x16x32_bf16 v[54:57], v[200:203], v[162:165], v[54:57]
	v_mfma_f32_16x16x32_bf16 v[50:53], v[208:211], v[162:165], v[50:53]
	v_mfma_f32_16x16x32_bf16 v[38:41], v[200:203], v[176:179], v[38:41]
	v_mfma_f32_16x16x32_bf16 v[34:37], v[208:211], v[176:179], v[34:37]
	v_mfma_f32_16x16x32_bf16 v[22:25], v[200:203], v[184:187], v[22:25]
	v_mfma_f32_16x16x32_bf16 v[18:21], v[208:211], v[184:187], v[18:21]
	v_mfma_f32_16x16x32_bf16 v[6:9], v[200:203], v[192:195], v[6:9]
	v_mfma_f32_16x16x32_bf16 v[2:5], v[208:211], v[192:195], v[2:5]
	v_mfma_f32_16x16x32_bf16 v[54:57], v[204:207], v[166:169], v[54:57]
	v_mfma_f32_16x16x32_bf16 v[50:53], v[214:217], v[166:169], v[50:53]
	v_mfma_f32_16x16x32_bf16 v[38:41], v[204:207], v[180:183], v[38:41]
	v_mfma_f32_16x16x32_bf16 v[34:37], v[214:217], v[180:183], v[34:37]
	v_mfma_f32_16x16x32_bf16 v[22:25], v[204:207], v[188:191], v[22:25]
	v_mfma_f32_16x16x32_bf16 v[18:21], v[214:217], v[188:191], v[18:21]
	v_mfma_f32_16x16x32_bf16 v[6:9], v[204:207], v[196:199], v[6:9]
	v_mfma_f32_16x16x32_bf16 v[2:5], v[214:217], v[196:199], v[2:5]
	s_setprio 0
	s_add_u32 s8, s8, 0x100
	s_addc_u32 s9, s9, 0
	s_add_u32 s53, s53, 0x100
	s_addc_u32 s54, s54, 0
	s_cmp_ge_i32 s55, s1
	s_mov_b32 s36, s55
	s_barrier
	s_cbranch_scc0 .LBB0_964
	s_branch .Lmy_pl1_exit
.LBB0_964:
	ds_read_b128 v[130:133], v172
	ds_read_b128 v[134:137], v172 offset:1024
	ds_read_b128 v[138:141], v172 offset:2048
	ds_read_b128 v[142:145], v172 offset:3072
	s_add_i32 s55, s36, 2
	s_add_u32 s37, s8, 0xfff80080
	s_addc_u32 s38, s9, -1
	s_cmp_eq_u32 s46, s36
	s_cselect_b32 s36, s52, s53
	s_cselect_b32 s39, s25, s38
	s_cselect_b32 s38, s27, s37
	s_cselect_b32 s37, s51, s54
	v_lshl_add_u64 v[200:201], s[8:9], 0, v[154:155]
	s_add_i32 m0, s23, 0xc000
	ds_read_b128 v[162:165], v173
	ds_read_b128 v[166:169], v173 offset:1024
	ds_read_b128 v[176:179], v173 offset:2048
	ds_read_b128 v[180:183], v173 offset:3072
	ds_read_b128 v[184:187], v173 offset:4096
	ds_read_b128 v[188:191], v173 offset:5120
	ds_read_b128 v[192:195], v173 offset:6144
	ds_read_b128 v[196:199], v173 offset:7168
	global_load_lds_dwordx4 v[200:201], off
	v_lshl_add_u64 v[200:201], s[8:9], 0, v[156:157]
	s_add_i32 m0, s23, 0xe000
	s_nop 0
	global_load_lds_dwordx4 v[200:201], off
	s_waitcnt lgkmcnt(8)
	s_barrier
	s_waitcnt lgkmcnt(0)
	s_setprio 1
	s_waitcnt lgkmcnt(0)
	v_mfma_f32_16x16x32_bf16 v[126:129], v[130:133], v[162:165], v[126:129]
	ds_read_b128 v[214:217], v174 offset:3072
	ds_read_b128 v[208:211], v174 offset:2048
	ds_read_b128 v[204:207], v174 offset:1024
	ds_read_b128 v[200:203], v174
	v_mfma_f32_16x16x32_bf16 v[122:125], v[138:141], v[162:165], v[122:125]
	v_mfma_f32_16x16x32_bf16 v[110:113], v[130:133], v[176:179], v[110:113]
	v_mfma_f32_16x16x32_bf16 v[106:109], v[138:141], v[176:179], v[106:109]
	v_mfma_f32_16x16x32_bf16 v[94:97], v[130:133], v[184:187], v[94:97]
	v_mfma_f32_16x16x32_bf16 v[90:93], v[138:141], v[184:187], v[90:93]
	v_mfma_f32_16x16x32_bf16 v[78:81], v[130:133], v[192:195], v[78:81]
	v_mfma_f32_16x16x32_bf16 v[74:77], v[138:141], v[192:195], v[74:77]
	v_mfma_f32_16x16x32_bf16 v[126:129], v[134:137], v[166:169], v[126:129]
	v_mfma_f32_16x16x32_bf16 v[122:125], v[142:145], v[166:169], v[122:125]
	v_mfma_f32_16x16x32_bf16 v[110:113], v[134:137], v[180:183], v[110:113]
	v_mfma_f32_16x16x32_bf16 v[106:109], v[142:145], v[180:183], v[106:109]
	v_mfma_f32_16x16x32_bf16 v[94:97], v[134:137], v[188:191], v[94:97]
	v_mfma_f32_16x16x32_bf16 v[90:93], v[142:145], v[188:191], v[90:93]
	v_mfma_f32_16x16x32_bf16 v[78:81], v[134:137], v[196:199], v[78:81]
	v_mfma_f32_16x16x32_bf16 v[74:77], v[142:145], v[196:199], v[74:77]
	s_setprio 0
	s_barrier
	s_add_i32 s56, s48, s5
	v_lshl_add_u64 v[218:219], s[36:37], 0, v[148:149]
	s_mov_b32 m0, s56
	global_load_lds_dwordx4 v[218:219], off
	v_lshl_add_u64 v[220:221], s[36:37], 0, v[152:153]
	s_add_i32 m0, s56, 0x2000
	s_nop 0
	global_load_lds_dwordx4 v[220:221], off
	s_barrier
	s_waitcnt lgkmcnt(0)
	s_setprio 1
	s_waitcnt lgkmcnt(0)
	v_mfma_f32_16x16x32_bf16 v[118:121], v[200:203], v[162:165], v[118:121]
	v_mfma_f32_16x16x32_bf16 v[114:117], v[208:211], v[162:165], v[114:117]
	ds_read_b128 v[162:165], v173 offset:16384
	v_mfma_f32_16x16x32_bf16 v[102:105], v[200:203], v[176:179], v[102:105]
	v_mfma_f32_16x16x32_bf16 v[98:101], v[208:211], v[176:179], v[98:101]
	ds_read_b128 v[176:179], v173 offset:18432
	v_mfma_f32_16x16x32_bf16 v[86:89], v[200:203], v[184:187], v[86:89]
	v_mfma_f32_16x16x32_bf16 v[82:85], v[208:211], v[184:187], v[82:85]
	ds_read_b128 v[184:187], v173 offset:20480
	v_mfma_f32_16x16x32_bf16 v[70:73], v[200:203], v[192:195], v[70:73]
	v_mfma_f32_16x16x32_bf16 v[66:69], v[208:211], v[192:195], v[66:69]
	ds_read_b128 v[192:195], v173 offset:22528
	v_mfma_f32_16x16x32_bf16 v[118:121], v[204:207], v[166:169], v[118:121]
	v_mfma_f32_16x16x32_bf16 v[114:117], v[214:217], v[166:169], v[114:117]
	ds_read_b128 v[166:169], v173 offset:17408
	v_mfma_f32_16x16x32_bf16 v[102:105], v[204:207], v[180:183], v[102:105]
	v_mfma_f32_16x16x32_bf16 v[98:101], v[214:217], v[180:183], v[98:101]
	ds_read_b128 v[180:183], v173 offset:19456
	v_mfma_f32_16x16x32_bf16 v[86:89], v[204:207], v[188:191], v[86:89]
	v_mfma_f32_16x16x32_bf16 v[82:85], v[214:217], v[188:191], v[82:85]
	ds_read_b128 v[188:191], v173 offset:21504
	v_mfma_f32_16x16x32_bf16 v[70:73], v[204:207], v[196:199], v[70:73]
	v_mfma_f32_16x16x32_bf16 v[66:69], v[214:217], v[196:199], v[66:69]
	ds_read_b128 v[196:199], v173 offset:23552
	s_setprio 0
	s_mov_b32 m0, s23
	v_lshl_add_u64 v[222:223], s[38:39], 0, v[146:147]
	s_barrier
	global_load_lds_dwordx4 v[222:223], off
	v_lshl_add_u64 v[224:225], s[38:39], 0, v[150:151]
	s_mov_b32 m0, s33
	s_nop 0
	global_load_lds_dwordx4 v[224:225], off
	s_barrier
	s_waitcnt lgkmcnt(0)
	s_setprio 1
	s_waitcnt lgkmcnt(0)
	v_mfma_f32_16x16x32_bf16 v[62:65], v[130:133], v[162:165], v[62:65]
	v_mfma_f32_16x16x32_bf16 v[58:61], v[138:141], v[162:165], v[58:61]
	v_mfma_f32_16x16x32_bf16 v[46:49], v[130:133], v[176:179], v[46:49]
	v_mfma_f32_16x16x32_bf16 v[42:45], v[138:141], v[176:179], v[42:45]
	v_mfma_f32_16x16x32_bf16 v[30:33], v[130:133], v[184:187], v[30:33]
	v_mfma_f32_16x16x32_bf16 v[26:29], v[138:141], v[184:187], v[26:29]
	v_mfma_f32_16x16x32_bf16 v[14:17], v[130:133], v[192:195], v[14:17]
	v_mfma_f32_16x16x32_bf16 v[10:13], v[138:141], v[192:195], v[10:13]
	v_mfma_f32_16x16x32_bf16 v[62:65], v[134:137], v[166:169], v[62:65]
	v_mfma_f32_16x16x32_bf16 v[58:61], v[142:145], v[166:169], v[58:61]
	v_mfma_f32_16x16x32_bf16 v[46:49], v[134:137], v[180:183], v[46:49]
	v_mfma_f32_16x16x32_bf16 v[42:45], v[142:145], v[180:183], v[42:45]
	v_mfma_f32_16x16x32_bf16 v[30:33], v[134:137], v[188:191], v[30:33]
	v_mfma_f32_16x16x32_bf16 v[26:29], v[142:145], v[188:191], v[26:29]
	v_mfma_f32_16x16x32_bf16 v[14:17], v[134:137], v[196:199], v[14:17]
	v_mfma_f32_16x16x32_bf16 v[10:13], v[142:145], v[196:199], v[10:13]
	s_setprio 0
	s_barrier
	s_add_u32 s56, s36, 0x80000
	s_addc_u32 s57, s37, 0
	s_add_i32 s58, s49, s5
	v_lshl_add_u64 v[130:131], s[56:57], 0, v[148:149]
	s_mov_b32 m0, s58
	s_nop 0
	global_load_lds_dwordx4 v[130:131], off
	v_lshl_add_u64 v[130:131], s[56:57], 0, v[152:153]
	s_add_i32 m0, s58, 0x2000
	s_nop 0
	global_load_lds_dwordx4 v[130:131], off
	s_waitcnt vmcnt(6)
	s_barrier
	s_setprio 1
	v_mfma_f32_16x16x32_bf16 v[54:57], v[200:203], v[162:165], v[54:57]
	v_mfma_f32_16x16x32_bf16 v[50:53], v[208:211], v[162:165], v[50:53]
	ds_read_b128 v[162:165], v173 offset:32768
	v_mfma_f32_16x16x32_bf16 v[38:41], v[200:203], v[176:179], v[38:41]
	v_mfma_f32_16x16x32_bf16 v[34:37], v[208:211], v[176:179], v[34:37]
	ds_read_b128 v[176:179], v173 offset:34816
	v_mfma_f32_16x16x32_bf16 v[22:25], v[200:203], v[184:187], v[22:25]
	v_mfma_f32_16x16x32_bf16 v[18:21], v[208:211], v[184:187], v[18:21]
	ds_read_b128 v[184:187], v173 offset:36864
	v_mfma_f32_16x16x32_bf16 v[6:9], v[200:203], v[192:195], v[6:9]
	v_mfma_f32_16x16x32_bf16 v[2:5], v[208:211], v[192:195], v[2:5]
	ds_read_b128 v[192:195], v173 offset:38912
	v_mfma_f32_16x16x32_bf16 v[54:57], v[204:207], v[166:169], v[54:57]
	v_mfma_f32_16x16x32_bf16 v[50:53], v[214:217], v[166:169], v[50:53]
	ds_read_b128 v[166:169], v173 offset:33792
	v_mfma_f32_16x16x32_bf16 v[38:41], v[204:207], v[180:183], v[38:41]
	v_mfma_f32_16x16x32_bf16 v[34:37], v[214:217], v[180:183], v[34:37]
	ds_read_b128 v[180:183], v173 offset:35840
	v_mfma_f32_16x16x32_bf16 v[22:25], v[204:207], v[188:191], v[22:25]
	v_mfma_f32_16x16x32_bf16 v[18:21], v[214:217], v[188:191], v[18:21]
	ds_read_b128 v[188:191], v173 offset:37888
	v_mfma_f32_16x16x32_bf16 v[6:9], v[204:207], v[196:199], v[6:9]
	v_mfma_f32_16x16x32_bf16 v[2:5], v[214:217], v[196:199], v[2:5]
	ds_read_b128 v[196:199], v173 offset:39936
	s_setprio 0
	s_add_i32 s56, 0, 0x18000
	v_add_u32_e32 v142, s56, v171
	s_barrier
	ds_read_b128 v[130:133], v142
	ds_read_b128 v[134:137], v142 offset:1024
	ds_read_b128 v[138:141], v142 offset:2048
	ds_read_b128 v[142:145], v142 offset:3072
	s_add_u32 s38, s38, 0x80000
	s_addc_u32 s39, s39, 0
	s_mov_b32 m0, s35
	v_lshl_add_u64 v[200:201], s[38:39], 0, v[146:147]
	global_load_lds_dwordx4 v[200:201], off
	v_lshl_add_u64 v[200:201], s[38:39], 0, v[150:151]
	s_mov_b32 m0, s40
	s_nop 0
	global_load_lds_dwordx4 v[200:201], off
	s_waitcnt lgkmcnt(8)
	s_barrier
	s_waitcnt lgkmcnt(0)
	s_setprio 1
	s_waitcnt lgkmcnt(0)
	v_mfma_f32_16x16x32_bf16 v[126:129], v[130:133], v[162:165], v[126:129]
	v_mfma_f32_16x16x32_bf16 v[122:125], v[138:141], v[162:165], v[122:125]
	v_mfma_f32_16x16x32_bf16 v[110:113], v[130:133], v[176:179], v[110:113]
	v_mfma_f32_16x16x32_bf16 v[106:109], v[138:141], v[176:179], v[106:109]
	v_mfma_f32_16x16x32_bf16 v[94:97], v[130:133], v[184:187], v[94:97]
	v_mfma_f32_16x16x32_bf16 v[90:93], v[138:141], v[184:187], v[90:93]
	v_mfma_f32_16x16x32_bf16 v[78:81], v[130:133], v[192:195], v[78:81]
	v_mfma_f32_16x16x32_bf16 v[74:77], v[138:141], v[192:195], v[74:77]
	v_mfma_f32_16x16x32_bf16 v[126:129], v[134:137], v[166:169], v[126:129]
	v_mfma_f32_16x16x32_bf16 v[122:125], v[142:145], v[166:169], v[122:125]
	v_mfma_f32_16x16x32_bf16 v[110:113], v[134:137], v[180:183], v[110:113]
	v_mfma_f32_16x16x32_bf16 v[106:109], v[142:145], v[180:183], v[106:109]
	v_mfma_f32_16x16x32_bf16 v[94:97], v[134:137], v[188:191], v[94:97]
	v_mfma_f32_16x16x32_bf16 v[90:93], v[142:145], v[188:191], v[90:93]
	v_mfma_f32_16x16x32_bf16 v[78:81], v[134:137], v[196:199], v[78:81]
	v_mfma_f32_16x16x32_bf16 v[74:77], v[142:145], v[196:199], v[74:77]
	s_setprio 0
	s_barrier
	s_add_i32 s38, 0, 0x1c000
	s_add_i32 s39, s56, s5
	v_add_u32_e32 v175, s38, v171
	v_lshl_add_u64 v[218:219], v[218:219], 0, s[18:19]
	s_mov_b32 m0, s39
	ds_read_b128 v[200:203], v175
	ds_read_b128 v[204:207], v175 offset:1024
	ds_read_b128 v[208:211], v175 offset:2048
	ds_read_b128 v[214:217], v175 offset:3072
	global_load_lds_dwordx4 v[218:219], off
	v_lshl_add_u64 v[218:219], v[220:221], 0, s[18:19]
	s_add_i32 m0, s39, 0x2000
	s_nop 0
	global_load_lds_dwordx4 v[218:219], off
	s_barrier
	s_waitcnt lgkmcnt(0)
	s_setprio 1
	s_waitcnt lgkmcnt(0)
	v_mfma_f32_16x16x32_bf16 v[118:121], v[200:203], v[162:165], v[118:121]
	v_mfma_f32_16x16x32_bf16 v[114:117], v[208:211], v[162:165], v[114:117]
	ds_read_b128 v[162:165], v173 offset:49152
	v_mfma_f32_16x16x32_bf16 v[102:105], v[200:203], v[176:179], v[102:105]
	v_mfma_f32_16x16x32_bf16 v[98:101], v[208:211], v[176:179], v[98:101]
	ds_read_b128 v[176:179], v173 offset:51200
	v_mfma_f32_16x16x32_bf16 v[86:89], v[200:203], v[184:187], v[86:89]
	v_mfma_f32_16x16x32_bf16 v[82:85], v[208:211], v[184:187], v[82:85]
	ds_read_b128 v[184:187], v173 offset:53248
	v_mfma_f32_16x16x32_bf16 v[70:73], v[200:203], v[192:195], v[70:73]
	v_mfma_f32_16x16x32_bf16 v[66:69], v[208:211], v[192:195], v[66:69]
	ds_read_b128 v[192:195], v173 offset:55296
	v_mfma_f32_16x16x32_bf16 v[118:121], v[204:207], v[166:169], v[118:121]
	v_mfma_f32_16x16x32_bf16 v[114:117], v[214:217], v[166:169], v[114:117]
	ds_read_b128 v[166:169], v173 offset:50176
	v_mfma_f32_16x16x32_bf16 v[102:105], v[204:207], v[180:183], v[102:105]
	v_mfma_f32_16x16x32_bf16 v[98:101], v[214:217], v[180:183], v[98:101]
	ds_read_b128 v[180:183], v173 offset:52224
	v_mfma_f32_16x16x32_bf16 v[86:89], v[204:207], v[188:191], v[86:89]
	v_mfma_f32_16x16x32_bf16 v[82:85], v[214:217], v[188:191], v[82:85]
	ds_read_b128 v[188:191], v173 offset:54272
	v_mfma_f32_16x16x32_bf16 v[70:73], v[204:207], v[196:199], v[70:73]
	v_mfma_f32_16x16x32_bf16 v[66:69], v[214:217], v[196:199], v[66:69]
	ds_read_b128 v[196:199], v173 offset:56320
	s_setprio 0
	s_mov_b32 m0, s44
	v_lshl_add_u64 v[218:219], v[222:223], 0, s[18:19]
	s_barrier
	global_load_lds_dwordx4 v[218:219], off
	v_lshl_add_u64 v[218:219], v[224:225], 0, s[18:19]
	s_mov_b32 m0, s45
	s_nop 0
	global_load_lds_dwordx4 v[218:219], off
	s_barrier
	s_waitcnt lgkmcnt(0)
	s_setprio 1
	s_waitcnt lgkmcnt(0)
	v_mfma_f32_16x16x32_bf16 v[62:65], v[130:133], v[162:165], v[62:65]
	v_mfma_f32_16x16x32_bf16 v[58:61], v[138:141], v[162:165], v[58:61]
	v_mfma_f32_16x16x32_bf16 v[46:49], v[130:133], v[176:179], v[46:49]
	v_mfma_f32_16x16x32_bf16 v[42:45], v[138:141], v[176:179], v[42:45]
	v_mfma_f32_16x16x32_bf16 v[30:33], v[130:133], v[184:187], v[30:33]
	v_mfma_f32_16x16x32_bf16 v[26:29], v[138:141], v[184:187], v[26:29]
	v_mfma_f32_16x16x32_bf16 v[14:17], v[130:133], v[192:195], v[14:17]
	v_mfma_f32_16x16x32_bf16 v[10:13], v[138:141], v[192:195], v[10:13]
	v_mfma_f32_16x16x32_bf16 v[62:65], v[134:137], v[166:169], v[62:65]
	v_mfma_f32_16x16x32_bf16 v[58:61], v[142:145], v[166:169], v[58:61]
	v_mfma_f32_16x16x32_bf16 v[46:49], v[134:137], v[180:183], v[46:49]
	v_mfma_f32_16x16x32_bf16 v[42:45], v[142:145], v[180:183], v[42:45]
	v_mfma_f32_16x16x32_bf16 v[30:33], v[134:137], v[188:191], v[30:33]
	v_mfma_f32_16x16x32_bf16 v[26:29], v[142:145], v[188:191], v[26:29]
	v_mfma_f32_16x16x32_bf16 v[14:17], v[134:137], v[196:199], v[14:17]
	v_mfma_f32_16x16x32_bf16 v[10:13], v[142:145], v[196:199], v[10:13]
	s_setprio 0
	s_barrier
	s_add_u32 s36, s36, 0x80080
	s_addc_u32 s37, s37, 0
	s_add_i32 s38, s38, s5
	v_lshl_add_u64 v[130:131], s[36:37], 0, v[148:149]
	s_mov_b32 m0, s38
	s_nop 0
	global_load_lds_dwordx4 v[130:131], off
	v_lshl_add_u64 v[130:131], s[36:37], 0, v[152:153]
	s_add_i32 m0, s38, 0x2000
	s_nop 0
	global_load_lds_dwordx4 v[130:131], off
	s_waitcnt vmcnt(6)
	s_barrier
	s_setprio 1
	v_mfma_f32_16x16x32_bf16 v[54:57], v[200:203], v[162:165], v[54:57]
	v_mfma_f32_16x16x32_bf16 v[50:53], v[208:211], v[162:165], v[50:53]
	v_mfma_f32_16x16x32_bf16 v[38:41], v[200:203], v[176:179], v[38:41]
	v_mfma_f32_16x16x32_bf16 v[34:37], v[208:211], v[176:179], v[34:37]
	v_mfma_f32_16x16x32_bf16 v[22:25], v[200:203], v[184:187], v[22:25]
	v_mfma_f32_16x16x32_bf16 v[18:21], v[208:211], v[184:187], v[18:21]
	v_mfma_f32_16x16x32_bf16 v[6:9], v[200:203], v[192:195], v[6:9]
	v_mfma_f32_16x16x32_bf16 v[2:5], v[208:211], v[192:195], v[2:5]
	v_mfma_f32_16x16x32_bf16 v[54:57], v[204:207], v[166:169], v[54:57]
	v_mfma_f32_16x16x32_bf16 v[50:53], v[214:217], v[166:169], v[50:53]
	v_mfma_f32_16x16x32_bf16 v[38:41], v[204:207], v[180:183], v[38:41]
	v_mfma_f32_16x16x32_bf16 v[34:37], v[214:217], v[180:183], v[34:37]
	v_mfma_f32_16x16x32_bf16 v[22:25], v[204:207], v[188:191], v[22:25]
	v_mfma_f32_16x16x32_bf16 v[18:21], v[214:217], v[188:191], v[18:21]
	v_mfma_f32_16x16x32_bf16 v[6:9], v[204:207], v[196:199], v[6:9]
	v_mfma_f32_16x16x32_bf16 v[2:5], v[214:217], v[196:199], v[2:5]
	s_setprio 0
	s_add_u32 s8, s8, 0x100
	s_addc_u32 s9, s9, 0
	s_add_u32 s53, s53, 0x100
	s_addc_u32 s54, s54, 0
	s_cmp_ge_i32 s55, s1
	s_mov_b32 s36, s55
	s_barrier
	s_cbranch_scc0 .LBB0_964

.Lmy_pl2_1553:
	s_add_i32 s71, s71, 2
	s_add_u32 s30, s28, 0x100
	s_addc_u32 s31, s29, 0
	s_and_b64 s[36:37], s[34:35], exec
	s_cselect_b32 s36, 0, s30
	s_cselect_b32 s37, 0, s31
	s_add_u32 s36, s22, s36
	s_addc_u32 s37, s23, s37
	s_add_u32 s72, s69, s28
	s_addc_u32 s73, s70, s29
	s_and_b64 s[28:29], s[34:35], exec
	s_cselect_b32 s29, s67, s73
	s_cselect_b32 s28, s68, s72
	s_mov_b32 m0, s42
	v_add_u32_e32 v191, s57, v204
	v_lshl_add_u64 v[230:231], s[28:29], 0, v[188:189]
	v_add_u32_e32 v197, s57, v205
	ds_read_b128 v[214:217], v191
	ds_read_b128 v[222:225], v191 offset:2048
	ds_read_b128 v[218:221], v197
	ds_read_b128 v[226:229], v197 offset:2048
	global_load_lds_dwordx4 v[230:231], off
	v_lshl_add_u64 v[232:233], s[28:29], 0, v[186:187]
	s_mov_b32 m0, s43
	s_waitcnt lgkmcnt(0)
	v_mfma_scale_f32_16x16x128_f8f6f4 v[174:177], v[2:9], v[26:33], 0, v211, v210 op_sel_hi:[0,0,0]
	global_load_lds_dwordx4 v[232:233], off
	s_barrier
	s_waitcnt lgkmcnt(0)
	v_mov_b32_e32 v193, v185
	v_mov_b32_e32 v195, v185
	v_mfma_scale_f32_16x16x128_f8f6f4 v[170:173], v[10:17], v[26:33], 0, v211, v210 op_sel_hi:[0,0,0]
	v_mfma_scale_f32_16x16x128_f8f6f4 v[166:169], v[2:9], v[18:25], 0, v211, v210 op_sel_hi:[0,0,0]
	v_mfma_scale_f32_16x16x128_f8f6f4 v[162:165], v[10:17], v[18:25], 0, v211, v210 op_sel_hi:[0,0,0]
	v_mfma_scale_f32_16x16x128_f8f6f4 v[142:145], v[2:9], v[42:49], 0, v211, v210 op_sel_hi:[0,0,0]
	v_mfma_scale_f32_16x16x128_f8f6f4 v[130:133], v[10:17], v[42:49], 0, v211, v210 op_sel_hi:[0,0,0]
	v_mfma_scale_f32_16x16x128_f8f6f4 v[118:121], v[2:9], v[34:41], 0, v211, v210 op_sel_hi:[0,0,0]
	v_mfma_scale_f32_16x16x128_f8f6f4 v[114:117], v[10:17], v[34:41], 0, v211, v210 op_sel_hi:[0,0,0]
	s_setprio 1
	v_mfma_scale_f32_16x16x128_f8f6f4 v[158:161], v[214:221], v[26:33], 0, v211, v210 op_sel_hi:[0,0,0]
	v_mfma_scale_f32_16x16x128_f8f6f4 v[154:157], v[222:229], v[26:33], 0, v211, v210 op_sel_hi:[0,0,0]
	ds_read_b128 v[30:33], v209 offset:18432
	ds_read_b128 v[26:29], v208 offset:18432
	v_mfma_scale_f32_16x16x128_f8f6f4 v[150:153], v[214:221], v[18:25], 0, v211, v210 op_sel_hi:[0,0,0]
	v_mfma_scale_f32_16x16x128_f8f6f4 v[146:149], v[222:229], v[18:25], 0, v211, v210 op_sel_hi:[0,0,0]
	ds_read_b128 v[22:25], v209 offset:16384
	ds_read_b128 v[18:21], v208 offset:16384
	v_mfma_scale_f32_16x16x128_f8f6f4 v[138:141], v[214:221], v[42:49], 0, v211, v210 op_sel_hi:[0,0,0]
	v_mfma_scale_f32_16x16x128_f8f6f4 v[134:137], v[222:229], v[42:49], 0, v211, v210 op_sel_hi:[0,0,0]
	ds_read_b128 v[46:49], v209 offset:22528
	ds_read_b128 v[42:45], v208 offset:22528
	v_mfma_scale_f32_16x16x128_f8f6f4 v[126:129], v[214:221], v[34:41], 0, v211, v210 op_sel_hi:[0,0,0]
	v_mfma_scale_f32_16x16x128_f8f6f4 v[122:125], v[222:229], v[34:41], 0, v211, v210 op_sel_hi:[0,0,0]
	ds_read_b128 v[38:41], v209 offset:20480
	ds_read_b128 v[34:37], v208 offset:20480
	s_setprio 0
	s_mov_b32 m0, s41
	s_barrier
	global_load_lds_dwordx4 v184, s[36:37]
	s_mov_b32 m0, s44
	v_mov_b32_e32 v191, v185
	global_load_lds_dwordx4 v190, s[36:37]
	s_barrier
	s_waitcnt lgkmcnt(0)
	v_lshl_add_u64 v[234:235], s[36:37], 0, v[184:185]
	v_lshl_add_u64 v[236:237], s[36:37], 0, v[190:191]
	s_setprio 1
	s_waitcnt lgkmcnt(0)
	v_mfma_scale_f32_16x16x128_f8f6f4 v[110:113], v[2:9], v[18:25], 0, v211, v210 op_sel_hi:[0,0,0]
	v_mfma_scale_f32_16x16x128_f8f6f4 v[102:105], v[10:17], v[18:25], 0, v211, v210 op_sel_hi:[0,0,0]
	v_mfma_scale_f32_16x16x128_f8f6f4 v[94:97], v[2:9], v[26:33], 0, v211, v210 op_sel_hi:[0,0,0]
	v_mfma_scale_f32_16x16x128_f8f6f4 v[86:89], v[10:17], v[26:33], 0, v211, v210 op_sel_hi:[0,0,0]
	v_mfma_scale_f32_16x16x128_f8f6f4 v[78:81], v[2:9], v[34:41], 0, v211, v210 op_sel_hi:[0,0,0]
	v_mfma_scale_f32_16x16x128_f8f6f4 v[70:73], v[10:17], v[34:41], 0, v211, v210 op_sel_hi:[0,0,0]
	v_mfma_scale_f32_16x16x128_f8f6f4 v[62:65], v[2:9], v[42:49], 0, v211, v210 op_sel_hi:[0,0,0]
	v_mfma_scale_f32_16x16x128_f8f6f4 v[54:57], v[10:17], v[42:49], 0, v211, v210 op_sel_hi:[0,0,0]
	s_setprio 0
	s_barrier
	s_add_u32 s34, s28, 0x40000
	s_addc_u32 s35, s29, 0
	s_mov_b32 m0, s59
	v_lshl_add_u64 v[2:3], s[34:35], 0, v[188:189]
	global_load_lds_dwordx4 v[2:3], off
	v_lshl_add_u64 v[2:3], s[34:35], 0, v[186:187]
	s_mov_b32 m0, s60
	s_nop 0
	global_load_lds_dwordx4 v[2:3], off
	s_waitcnt vmcnt(6)
	s_barrier
	s_setprio 1
	v_mfma_scale_f32_16x16x128_f8f6f4 v[106:109], v[214:221], v[18:25], 0, v211, v210 op_sel_hi:[0,0,0]
	v_add_u32_e32 v14, s61, v205
	v_add_u32_e32 v6, s61, v204
	ds_read_b128 v[10:13], v6 offset:2048
	ds_read_b128 v[2:5], v6
	ds_read_b128 v[6:9], v14
	ds_read_b128 v[14:17], v14 offset:2048
	v_mfma_scale_f32_16x16x128_f8f6f4 v[98:101], v[222:229], v[18:25], 0, v211, v210 op_sel_hi:[0,0,0]
	ds_read_b128 v[22:25], v209 offset:32768
	ds_read_b128 v[18:21], v208 offset:32768
	v_mfma_scale_f32_16x16x128_f8f6f4 v[90:93], v[214:221], v[26:33], 0, v211, v210 op_sel_hi:[0,0,0]
	v_mfma_scale_f32_16x16x128_f8f6f4 v[82:85], v[222:229], v[26:33], 0, v211, v210 op_sel_hi:[0,0,0]
	ds_read_b128 v[30:33], v209 offset:34816
	ds_read_b128 v[26:29], v208 offset:34816
	v_mfma_scale_f32_16x16x128_f8f6f4 v[74:77], v[214:221], v[34:41], 0, v211, v210 op_sel_hi:[0,0,0]
	v_mfma_scale_f32_16x16x128_f8f6f4 v[66:69], v[222:229], v[34:41], 0, v211, v210 op_sel_hi:[0,0,0]
	ds_read_b128 v[38:41], v209 offset:36864
	ds_read_b128 v[34:37], v208 offset:36864
	v_mfma_scale_f32_16x16x128_f8f6f4 v[58:61], v[214:221], v[42:49], 0, v211, v210 op_sel_hi:[0,0,0]
	v_mfma_scale_f32_16x16x128_f8f6f4 v[50:53], v[222:229], v[42:49], 0, v211, v210 op_sel_hi:[0,0,0]
	ds_read_b128 v[46:49], v209 offset:38912
	ds_read_b128 v[42:45], v208 offset:38912
	s_setprio 0
	s_barrier
	s_mov_b32 m0, s45
	v_lshl_add_u64 v[214:215], s[36:37], 0, v[192:193]
	global_load_lds_dwordx4 v[214:215], off
	v_lshl_add_u64 v[214:215], s[36:37], 0, v[194:195]
	s_mov_b32 m0, s46
	s_nop 0
	global_load_lds_dwordx4 v[214:215], off
	s_waitcnt lgkmcnt(8)
	s_barrier
	s_waitcnt lgkmcnt(0)
	s_setprio 1
	s_waitcnt lgkmcnt(0)
	v_mfma_scale_f32_16x16x128_f8f6f4 v[174:177], v[2:9], v[18:25], v[174:177], v211, v210 op_sel_hi:[0,0,0]
	v_add_u32_e32 v193, s62, v205
	ds_read_b128 v[226:229], v193 offset:2048
	ds_read_b128 v[218:221], v193
	v_add_u32_e32 v191, s62, v204
	ds_read_b128 v[222:225], v191 offset:2048
	ds_read_b128 v[214:217], v191
	v_mfma_scale_f32_16x16x128_f8f6f4 v[170:173], v[10:17], v[18:25], v[170:173], v211, v210 op_sel_hi:[0,0,0]
	v_mfma_scale_f32_16x16x128_f8f6f4 v[166:169], v[2:9], v[26:33], v[166:169], v211, v210 op_sel_hi:[0,0,0]
	v_mfma_scale_f32_16x16x128_f8f6f4 v[162:165], v[10:17], v[26:33], v[162:165], v211, v210 op_sel_hi:[0,0,0]
	v_mfma_scale_f32_16x16x128_f8f6f4 v[142:145], v[2:9], v[34:41], v[142:145], v211, v210 op_sel_hi:[0,0,0]
	v_mfma_scale_f32_16x16x128_f8f6f4 v[130:133], v[10:17], v[34:41], v[130:133], v211, v210 op_sel_hi:[0,0,0]
	v_mfma_scale_f32_16x16x128_f8f6f4 v[118:121], v[2:9], v[42:49], v[118:121], v211, v210 op_sel_hi:[0,0,0]
	v_mfma_scale_f32_16x16x128_f8f6f4 v[114:117], v[10:17], v[42:49], v[114:117], v211, v210 op_sel_hi:[0,0,0]
	s_setprio 0
	s_barrier
	s_mov_b32 m0, s63
	v_lshl_add_u64 v[230:231], v[230:231], 0, s[12:13]
	global_load_lds_dwordx4 v[230:231], off
	v_lshl_add_u64 v[230:231], v[232:233], 0, s[12:13]
	s_add_i32 m0, s63, 0x2000
	s_nop 0
	global_load_lds_dwordx4 v[230:231], off
	s_barrier
	s_waitcnt lgkmcnt(0)
	s_setprio 1
	s_waitcnt lgkmcnt(0)
	v_mfma_scale_f32_16x16x128_f8f6f4 v[158:161], v[214:221], v[18:25], v[158:161], v211, v210 op_sel_hi:[0,0,0]
	v_mfma_scale_f32_16x16x128_f8f6f4 v[154:157], v[222:229], v[18:25], v[154:157], v211, v210 op_sel_hi:[0,0,0]
	ds_read_b128 v[22:25], v209 offset:49152
	ds_read_b128 v[18:21], v208 offset:49152
	v_mfma_scale_f32_16x16x128_f8f6f4 v[150:153], v[214:221], v[26:33], v[150:153], v211, v210 op_sel_hi:[0,0,0]
	v_mfma_scale_f32_16x16x128_f8f6f4 v[146:149], v[222:229], v[26:33], v[146:149], v211, v210 op_sel_hi:[0,0,0]
	ds_read_b128 v[30:33], v209 offset:51200
	ds_read_b128 v[26:29], v208 offset:51200
	v_mfma_scale_f32_16x16x128_f8f6f4 v[138:141], v[214:221], v[34:41], v[138:141], v211, v210 op_sel_hi:[0,0,0]
	v_mfma_scale_f32_16x16x128_f8f6f4 v[134:137], v[222:229], v[34:41], v[134:137], v211, v210 op_sel_hi:[0,0,0]
	ds_read_b128 v[38:41], v209 offset:53248
	ds_read_b128 v[34:37], v208 offset:53248
	v_mfma_scale_f32_16x16x128_f8f6f4 v[126:129], v[214:221], v[42:49], v[126:129], v211, v210 op_sel_hi:[0,0,0]
	v_mfma_scale_f32_16x16x128_f8f6f4 v[122:125], v[222:229], v[42:49], v[122:125], v211, v210 op_sel_hi:[0,0,0]
	ds_read_b128 v[46:49], v209 offset:55296
	ds_read_b128 v[42:45], v208 offset:55296
	s_setprio 0
	s_mov_b32 m0, s49
	v_lshl_add_u64 v[230:231], v[234:235], 0, s[12:13]
	s_barrier
	global_load_lds_dwordx4 v[230:231], off
	v_lshl_add_u64 v[230:231], v[236:237], 0, s[12:13]
	s_mov_b32 m0, s50
	s_nop 0
	global_load_lds_dwordx4 v[230:231], off
	s_barrier
	s_waitcnt lgkmcnt(0)
	s_setprio 1
	s_waitcnt lgkmcnt(0)
	v_mfma_scale_f32_16x16x128_f8f6f4 v[110:113], v[2:9], v[18:25], v[110:113], v211, v210 op_sel_hi:[0,0,0]
	v_mfma_scale_f32_16x16x128_f8f6f4 v[102:105], v[10:17], v[18:25], v[102:105], v211, v210 op_sel_hi:[0,0,0]
	v_mfma_scale_f32_16x16x128_f8f6f4 v[94:97], v[2:9], v[26:33], v[94:97], v211, v210 op_sel_hi:[0,0,0]
	v_mfma_scale_f32_16x16x128_f8f6f4 v[86:89], v[10:17], v[26:33], v[86:89], v211, v210 op_sel_hi:[0,0,0]
	v_mfma_scale_f32_16x16x128_f8f6f4 v[78:81], v[2:9], v[34:41], v[78:81], v211, v210 op_sel_hi:[0,0,0]
	v_mfma_scale_f32_16x16x128_f8f6f4 v[70:73], v[10:17], v[34:41], v[70:73], v211, v210 op_sel_hi:[0,0,0]
	v_mfma_scale_f32_16x16x128_f8f6f4 v[62:65], v[2:9], v[42:49], v[62:65], v211, v210 op_sel_hi:[0,0,0]
	v_mfma_scale_f32_16x16x128_f8f6f4 v[54:57], v[10:17], v[42:49], v[54:57], v211, v210 op_sel_hi:[0,0,0]
	s_setprio 0
	s_barrier
	s_add_u32 s28, s28, 0x40080
	s_addc_u32 s29, s29, 0
	s_add_i32 s34, s62, s40
	v_lshl_add_u64 v[2:3], s[28:29], 0, v[188:189]
	s_mov_b32 m0, s34
	s_nop 0
	global_load_lds_dwordx4 v[2:3], off
	v_lshl_add_u64 v[2:3], s[28:29], 0, v[186:187]
	s_add_i32 m0, s34, 0x2000
	s_nop 0
	global_load_lds_dwordx4 v[2:3], off
	s_waitcnt vmcnt(6)
	s_barrier
	s_setprio 1
	v_mfma_scale_f32_16x16x128_f8f6f4 v[106:109], v[214:221], v[18:25], v[106:109], v211, v210 op_sel_hi:[0,0,0]
	v_mfma_scale_f32_16x16x128_f8f6f4 v[98:101], v[222:229], v[18:25], v[98:101], v211, v210 op_sel_hi:[0,0,0]
	v_mfma_scale_f32_16x16x128_f8f6f4 v[90:93], v[214:221], v[26:33], v[90:93], v211, v210 op_sel_hi:[0,0,0]
	v_mfma_scale_f32_16x16x128_f8f6f4 v[82:85], v[222:229], v[26:33], v[82:85], v211, v210 op_sel_hi:[0,0,0]
	v_mfma_scale_f32_16x16x128_f8f6f4 v[74:77], v[214:221], v[34:41], v[74:77], v211, v210 op_sel_hi:[0,0,0]
	v_mfma_scale_f32_16x16x128_f8f6f4 v[66:69], v[222:229], v[34:41], v[66:69], v211, v210 op_sel_hi:[0,0,0]
	v_mfma_scale_f32_16x16x128_f8f6f4 v[58:61], v[214:221], v[42:49], v[58:61], v211, v210 op_sel_hi:[0,0,0]
	v_mfma_scale_f32_16x16x128_f8f6f4 v[50:53], v[222:229], v[42:49], v[50:53], v211, v210 op_sel_hi:[0,0,0]
	s_setprio 0
	s_cmp_ge_i32 s71, s39
	s_barrier
	s_cbranch_scc1 .LBB0_1546
	s_mov_b64 s[28:29], s[30:31]
	s_branch .LBB0_1551

.LBB0_1553:
	s_add_i32 s71, s71, 2
	s_add_u32 s30, s28, 0x100
	s_addc_u32 s31, s29, 0
	s_and_b64 s[36:37], s[34:35], exec
	s_cselect_b32 s36, 0, s30
	s_cselect_b32 s37, 0, s31
	s_add_u32 s36, s22, s36
	s_addc_u32 s37, s23, s37
	s_add_u32 s72, s69, s28
	s_addc_u32 s73, s70, s29
	s_and_b64 s[28:29], s[34:35], exec
	s_cselect_b32 s29, s67, s73
	s_cselect_b32 s28, s68, s72
	s_mov_b32 m0, s42
	v_add_u32_e32 v191, s57, v204
	v_lshl_add_u64 v[230:231], s[28:29], 0, v[188:189]
	v_add_u32_e32 v197, s57, v205
	ds_read_b128 v[214:217], v191
	ds_read_b128 v[222:225], v191 offset:2048
	ds_read_b128 v[218:221], v197
	ds_read_b128 v[226:229], v197 offset:2048
	global_load_lds_dwordx4 v[230:231], off
	v_lshl_add_u64 v[232:233], s[28:29], 0, v[186:187]
	s_mov_b32 m0, s43
	s_waitcnt lgkmcnt(0)
	v_mfma_scale_f32_16x16x128_f8f6f4 v[174:177], v[2:9], v[26:33], v[174:177], v211, v210 op_sel_hi:[0,0,0]
	global_load_lds_dwordx4 v[232:233], off
	s_barrier
	s_waitcnt lgkmcnt(0)
	v_mov_b32_e32 v193, v185
	v_mov_b32_e32 v195, v185
	v_mfma_scale_f32_16x16x128_f8f6f4 v[170:173], v[10:17], v[26:33], v[170:173], v211, v210 op_sel_hi:[0,0,0]
	v_mfma_scale_f32_16x16x128_f8f6f4 v[166:169], v[2:9], v[18:25], v[166:169], v211, v210 op_sel_hi:[0,0,0]
	v_mfma_scale_f32_16x16x128_f8f6f4 v[162:165], v[10:17], v[18:25], v[162:165], v211, v210 op_sel_hi:[0,0,0]
	v_mfma_scale_f32_16x16x128_f8f6f4 v[142:145], v[2:9], v[42:49], v[142:145], v211, v210 op_sel_hi:[0,0,0]
	v_mfma_scale_f32_16x16x128_f8f6f4 v[130:133], v[10:17], v[42:49], v[130:133], v211, v210 op_sel_hi:[0,0,0]
	v_mfma_scale_f32_16x16x128_f8f6f4 v[118:121], v[2:9], v[34:41], v[118:121], v211, v210 op_sel_hi:[0,0,0]
	v_mfma_scale_f32_16x16x128_f8f6f4 v[114:117], v[10:17], v[34:41], v[114:117], v211, v210 op_sel_hi:[0,0,0]
	s_setprio 1
	v_mfma_scale_f32_16x16x128_f8f6f4 v[158:161], v[214:221], v[26:33], v[158:161], v211, v210 op_sel_hi:[0,0,0]
	v_mfma_scale_f32_16x16x128_f8f6f4 v[154:157], v[222:229], v[26:33], v[154:157], v211, v210 op_sel_hi:[0,0,0]
	ds_read_b128 v[30:33], v209 offset:18432
	ds_read_b128 v[26:29], v208 offset:18432
	v_mfma_scale_f32_16x16x128_f8f6f4 v[150:153], v[214:221], v[18:25], v[150:153], v211, v210 op_sel_hi:[0,0,0]
	v_mfma_scale_f32_16x16x128_f8f6f4 v[146:149], v[222:229], v[18:25], v[146:149], v211, v210 op_sel_hi:[0,0,0]
	ds_read_b128 v[22:25], v209 offset:16384
	ds_read_b128 v[18:21], v208 offset:16384
	v_mfma_scale_f32_16x16x128_f8f6f4 v[138:141], v[214:221], v[42:49], v[138:141], v211, v210 op_sel_hi:[0,0,0]
	v_mfma_scale_f32_16x16x128_f8f6f4 v[134:137], v[222:229], v[42:49], v[134:137], v211, v210 op_sel_hi:[0,0,0]
	ds_read_b128 v[46:49], v209 offset:22528
	ds_read_b128 v[42:45], v208 offset:22528
	v_mfma_scale_f32_16x16x128_f8f6f4 v[126:129], v[214:221], v[34:41], v[126:129], v211, v210 op_sel_hi:[0,0,0]
	v_mfma_scale_f32_16x16x128_f8f6f4 v[122:125], v[222:229], v[34:41], v[122:125], v211, v210 op_sel_hi:[0,0,0]
	ds_read_b128 v[38:41], v209 offset:20480
	ds_read_b128 v[34:37], v208 offset:20480
	s_setprio 0
	s_mov_b32 m0, s41
	s_barrier
	global_load_lds_dwordx4 v184, s[36:37]
	s_mov_b32 m0, s44
	v_mov_b32_e32 v191, v185
	global_load_lds_dwordx4 v190, s[36:37]
	s_barrier
	s_waitcnt lgkmcnt(0)
	v_lshl_add_u64 v[234:235], s[36:37], 0, v[184:185]
	v_lshl_add_u64 v[236:237], s[36:37], 0, v[190:191]
	s_setprio 1
	s_waitcnt lgkmcnt(0)
	v_mfma_scale_f32_16x16x128_f8f6f4 v[110:113], v[2:9], v[18:25], v[110:113], v211, v210 op_sel_hi:[0,0,0]
	v_mfma_scale_f32_16x16x128_f8f6f4 v[102:105], v[10:17], v[18:25], v[102:105], v211, v210 op_sel_hi:[0,0,0]
	v_mfma_scale_f32_16x16x128_f8f6f4 v[94:97], v[2:9], v[26:33], v[94:97], v211, v210 op_sel_hi:[0,0,0]
	v_mfma_scale_f32_16x16x128_f8f6f4 v[86:89], v[10:17], v[26:33], v[86:89], v211, v210 op_sel_hi:[0,0,0]
	v_mfma_scale_f32_16x16x128_f8f6f4 v[78:81], v[2:9], v[34:41], v[78:81], v211, v210 op_sel_hi:[0,0,0]
	v_mfma_scale_f32_16x16x128_f8f6f4 v[70:73], v[10:17], v[34:41], v[70:73], v211, v210 op_sel_hi:[0,0,0]
	v_mfma_scale_f32_16x16x128_f8f6f4 v[62:65], v[2:9], v[42:49], v[62:65], v211, v210 op_sel_hi:[0,0,0]
	v_mfma_scale_f32_16x16x128_f8f6f4 v[54:57], v[10:17], v[42:49], v[54:57], v211, v210 op_sel_hi:[0,0,0]
	s_setprio 0
	s_barrier
	s_add_u32 s34, s28, 0x40000
	s_addc_u32 s35, s29, 0
	s_mov_b32 m0, s59
	v_lshl_add_u64 v[2:3], s[34:35], 0, v[188:189]
	global_load_lds_dwordx4 v[2:3], off
	v_lshl_add_u64 v[2:3], s[34:35], 0, v[186:187]
	s_mov_b32 m0, s60
	s_nop 0
	global_load_lds_dwordx4 v[2:3], off
	s_waitcnt vmcnt(6)
	s_barrier
	s_setprio 1
	v_mfma_scale_f32_16x16x128_f8f6f4 v[106:109], v[214:221], v[18:25], v[106:109], v211, v210 op_sel_hi:[0,0,0]
	v_add_u32_e32 v14, s61, v205
	v_add_u32_e32 v6, s61, v204
	ds_read_b128 v[10:13], v6 offset:2048
	ds_read_b128 v[2:5], v6
	ds_read_b128 v[6:9], v14
	ds_read_b128 v[14:17], v14 offset:2048
	v_mfma_scale_f32_16x16x128_f8f6f4 v[98:101], v[222:229], v[18:25], v[98:101], v211, v210 op_sel_hi:[0,0,0]
	ds_read_b128 v[22:25], v209 offset:32768
	ds_read_b128 v[18:21], v208 offset:32768
	v_mfma_scale_f32_16x16x128_f8f6f4 v[90:93], v[214:221], v[26:33], v[90:93], v211, v210 op_sel_hi:[0,0,0]
	v_mfma_scale_f32_16x16x128_f8f6f4 v[82:85], v[222:229], v[26:33], v[82:85], v211, v210 op_sel_hi:[0,0,0]
	ds_read_b128 v[30:33], v209 offset:34816
	ds_read_b128 v[26:29], v208 offset:34816
	v_mfma_scale_f32_16x16x128_f8f6f4 v[74:77], v[214:221], v[34:41], v[74:77], v211, v210 op_sel_hi:[0,0,0]
	v_mfma_scale_f32_16x16x128_f8f6f4 v[66:69], v[222:229], v[34:41], v[66:69], v211, v210 op_sel_hi:[0,0,0]
	ds_read_b128 v[38:41], v209 offset:36864
	ds_read_b128 v[34:37], v208 offset:36864
	v_mfma_scale_f32_16x16x128_f8f6f4 v[58:61], v[214:221], v[42:49], v[58:61], v211, v210 op_sel_hi:[0,0,0]
	v_mfma_scale_f32_16x16x128_f8f6f4 v[50:53], v[222:229], v[42:49], v[50:53], v211, v210 op_sel_hi:[0,0,0]
	ds_read_b128 v[46:49], v209 offset:38912
	ds_read_b128 v[42:45], v208 offset:38912
	s_setprio 0
	s_barrier
	s_mov_b32 m0, s45
	v_lshl_add_u64 v[214:215], s[36:37], 0, v[192:193]
	global_load_lds_dwordx4 v[214:215], off
	v_lshl_add_u64 v[214:215], s[36:37], 0, v[194:195]
	s_mov_b32 m0, s46
	s_nop 0
	global_load_lds_dwordx4 v[214:215], off
	s_waitcnt lgkmcnt(8)
	s_barrier
	s_waitcnt lgkmcnt(0)
	s_setprio 1
	s_waitcnt lgkmcnt(0)
	v_mfma_scale_f32_16x16x128_f8f6f4 v[174:177], v[2:9], v[18:25], v[174:177], v211, v210 op_sel_hi:[0,0,0]
	v_add_u32_e32 v193, s62, v205
	ds_read_b128 v[226:229], v193 offset:2048
	ds_read_b128 v[218:221], v193
	v_add_u32_e32 v191, s62, v204
	ds_read_b128 v[222:225], v191 offset:2048
	ds_read_b128 v[214:217], v191
	v_mfma_scale_f32_16x16x128_f8f6f4 v[170:173], v[10:17], v[18:25], v[170:173], v211, v210 op_sel_hi:[0,0,0]
	v_mfma_scale_f32_16x16x128_f8f6f4 v[166:169], v[2:9], v[26:33], v[166:169], v211, v210 op_sel_hi:[0,0,0]
	v_mfma_scale_f32_16x16x128_f8f6f4 v[162:165], v[10:17], v[26:33], v[162:165], v211, v210 op_sel_hi:[0,0,0]
	v_mfma_scale_f32_16x16x128_f8f6f4 v[142:145], v[2:9], v[34:41], v[142:145], v211, v210 op_sel_hi:[0,0,0]
	v_mfma_scale_f32_16x16x128_f8f6f4 v[130:133], v[10:17], v[34:41], v[130:133], v211, v210 op_sel_hi:[0,0,0]
	v_mfma_scale_f32_16x16x128_f8f6f4 v[118:121], v[2:9], v[42:49], v[118:121], v211, v210 op_sel_hi:[0,0,0]
	v_mfma_scale_f32_16x16x128_f8f6f4 v[114:117], v[10:17], v[42:49], v[114:117], v211, v210 op_sel_hi:[0,0,0]
	s_setprio 0
	s_barrier
	s_mov_b32 m0, s63
	v_lshl_add_u64 v[230:231], v[230:231], 0, s[12:13]
	global_load_lds_dwordx4 v[230:231], off
	v_lshl_add_u64 v[230:231], v[232:233], 0, s[12:13]
	s_add_i32 m0, s63, 0x2000
	s_nop 0
	global_load_lds_dwordx4 v[230:231], off
	s_barrier
	s_waitcnt lgkmcnt(0)
	s_setprio 1
	s_waitcnt lgkmcnt(0)
	v_mfma_scale_f32_16x16x128_f8f6f4 v[158:161], v[214:221], v[18:25], v[158:161], v211, v210 op_sel_hi:[0,0,0]
	v_mfma_scale_f32_16x16x128_f8f6f4 v[154:157], v[222:229], v[18:25], v[154:157], v211, v210 op_sel_hi:[0,0,0]
	ds_read_b128 v[22:25], v209 offset:49152
	ds_read_b128 v[18:21], v208 offset:49152
	v_mfma_scale_f32_16x16x128_f8f6f4 v[150:153], v[214:221], v[26:33], v[150:153], v211, v210 op_sel_hi:[0,0,0]
	v_mfma_scale_f32_16x16x128_f8f6f4 v[146:149], v[222:229], v[26:33], v[146:149], v211, v210 op_sel_hi:[0,0,0]
	ds_read_b128 v[30:33], v209 offset:51200
	ds_read_b128 v[26:29], v208 offset:51200
	v_mfma_scale_f32_16x16x128_f8f6f4 v[138:141], v[214:221], v[34:41], v[138:141], v211, v210 op_sel_hi:[0,0,0]
	v_mfma_scale_f32_16x16x128_f8f6f4 v[134:137], v[222:229], v[34:41], v[134:137], v211, v210 op_sel_hi:[0,0,0]
	ds_read_b128 v[38:41], v209 offset:53248
	ds_read_b128 v[34:37], v208 offset:53248
	v_mfma_scale_f32_16x16x128_f8f6f4 v[126:129], v[214:221], v[42:49], v[126:129], v211, v210 op_sel_hi:[0,0,0]
	v_mfma_scale_f32_16x16x128_f8f6f4 v[122:125], v[222:229], v[42:49], v[122:125], v211, v210 op_sel_hi:[0,0,0]
	ds_read_b128 v[46:49], v209 offset:55296
	ds_read_b128 v[42:45], v208 offset:55296
	s_setprio 0
	s_mov_b32 m0, s49
	v_lshl_add_u64 v[230:231], v[234:235], 0, s[12:13]
	s_barrier
	global_load_lds_dwordx4 v[230:231], off
	v_lshl_add_u64 v[230:231], v[236:237], 0, s[12:13]
	s_mov_b32 m0, s50
	s_nop 0
	global_load_lds_dwordx4 v[230:231], off
	s_barrier
	s_waitcnt lgkmcnt(0)
	s_setprio 1
	s_waitcnt lgkmcnt(0)
	v_mfma_scale_f32_16x16x128_f8f6f4 v[110:113], v[2:9], v[18:25], v[110:113], v211, v210 op_sel_hi:[0,0,0]
	v_mfma_scale_f32_16x16x128_f8f6f4 v[102:105], v[10:17], v[18:25], v[102:105], v211, v210 op_sel_hi:[0,0,0]
	v_mfma_scale_f32_16x16x128_f8f6f4 v[94:97], v[2:9], v[26:33], v[94:97], v211, v210 op_sel_hi:[0,0,0]
	v_mfma_scale_f32_16x16x128_f8f6f4 v[86:89], v[10:17], v[26:33], v[86:89], v211, v210 op_sel_hi:[0,0,0]
	v_mfma_scale_f32_16x16x128_f8f6f4 v[78:81], v[2:9], v[34:41], v[78:81], v211, v210 op_sel_hi:[0,0,0]
	v_mfma_scale_f32_16x16x128_f8f6f4 v[70:73], v[10:17], v[34:41], v[70:73], v211, v210 op_sel_hi:[0,0,0]
	v_mfma_scale_f32_16x16x128_f8f6f4 v[62:65], v[2:9], v[42:49], v[62:65], v211, v210 op_sel_hi:[0,0,0]
	v_mfma_scale_f32_16x16x128_f8f6f4 v[54:57], v[10:17], v[42:49], v[54:57], v211, v210 op_sel_hi:[0,0,0]
	s_setprio 0
	s_barrier
	s_add_u32 s28, s28, 0x40080
	s_addc_u32 s29, s29, 0
	s_add_i32 s34, s62, s40
	v_lshl_add_u64 v[2:3], s[28:29], 0, v[188:189]
	s_mov_b32 m0, s34
	s_nop 0
	global_load_lds_dwordx4 v[2:3], off
	v_lshl_add_u64 v[2:3], s[28:29], 0, v[186:187]
	s_add_i32 m0, s34, 0x2000
	s_nop 0
	global_load_lds_dwordx4 v[2:3], off
	s_waitcnt vmcnt(6)
	s_barrier
	s_setprio 1
	v_mfma_scale_f32_16x16x128_f8f6f4 v[106:109], v[214:221], v[18:25], v[106:109], v211, v210 op_sel_hi:[0,0,0]
	v_mfma_scale_f32_16x16x128_f8f6f4 v[98:101], v[222:229], v[18:25], v[98:101], v211, v210 op_sel_hi:[0,0,0]
	v_mfma_scale_f32_16x16x128_f8f6f4 v[90:93], v[214:221], v[26:33], v[90:93], v211, v210 op_sel_hi:[0,0,0]
	v_mfma_scale_f32_16x16x128_f8f6f4 v[82:85], v[222:229], v[26:33], v[82:85], v211, v210 op_sel_hi:[0,0,0]
	v_mfma_scale_f32_16x16x128_f8f6f4 v[74:77], v[214:221], v[34:41], v[74:77], v211, v210 op_sel_hi:[0,0,0]
	v_mfma_scale_f32_16x16x128_f8f6f4 v[66:69], v[222:229], v[34:41], v[66:69], v211, v210 op_sel_hi:[0,0,0]
	v_mfma_scale_f32_16x16x128_f8f6f4 v[58:61], v[214:221], v[42:49], v[58:61], v211, v210 op_sel_hi:[0,0,0]
	v_mfma_scale_f32_16x16x128_f8f6f4 v[50:53], v[222:229], v[42:49], v[50:53], v211, v210 op_sel_hi:[0,0,0]
	s_setprio 0
	s_cmp_ge_i32 s71, s39
	s_barrier
	s_cbranch_scc1 .LBB0_1546
	s_mov_b64 s[28:29], s[30:31]
	s_branch .LBB0_1551

.Lmy_pl3_1675:
	s_add_i32 s59, s59, 2
	s_add_u32 s24, s22, 0x100
	s_addc_u32 s25, s23, 0
	s_and_b64 s[28:29], s[26:27], exec
	s_cselect_b32 s28, 0, s24
	s_cselect_b32 s29, 0, s25
	s_add_u32 s28, s12, s28
	s_addc_u32 s29, s13, s29
	s_add_u32 s60, s57, s22
	s_addc_u32 s61, s58, s23
	s_and_b64 s[22:23], s[26:27], exec
	s_cselect_b32 s23, s55, s61
	s_cselect_b32 s22, s56, s60
	s_mov_b32 m0, s5
	s_waitcnt lgkmcnt(0)
	v_mfma_scale_f32_16x16x128_f8f6f4 v[222:225], v[2:9], v[42:49], 0, v209, v208 op_sel_hi:[0,0,0]
	v_lshl_add_u64 v[238:239], s[22:23], 0, v[188:189]
	v_add_u32_e32 v191, s46, v203
	v_lshl_add_u64 v[240:241], s[22:23], 0, v[186:187]
	v_mov_b32_e32 v193, v185
	v_mov_b32_e32 v195, v185
	s_nop 1
	v_add_u32_e32 v142, s46, v202
	v_mfma_scale_f32_16x16x128_f8f6f4 v[226:229], v[10:17], v[42:49], 0, v209, v208 op_sel_hi:[0,0,0]
	s_nop 6
	ds_read_b128 v[138:141], v142
	ds_read_b128 v[214:217], v142 offset:2048
	ds_read_b128 v[142:145], v191
	ds_read_b128 v[218:221], v191 offset:2048
	global_load_lds_dwordx4 v[238:239], off
	s_mov_b32 m0, s31
	s_nop 0
	global_load_lds_dwordx4 v[240:241], off
	v_mfma_scale_f32_16x16x128_f8f6f4 v[174:177], v[2:9], v[26:33], 0, v209, v208 op_sel_hi:[0,0,0]
	s_barrier
	s_waitcnt lgkmcnt(0)
	v_mfma_scale_f32_16x16x128_f8f6f4 v[170:173], v[10:17], v[26:33], 0, v209, v208 op_sel_hi:[0,0,0]
	v_mfma_scale_f32_16x16x128_f8f6f4 v[166:169], v[2:9], v[18:25], 0, v209, v208 op_sel_hi:[0,0,0]
	v_mfma_scale_f32_16x16x128_f8f6f4 v[162:165], v[10:17], v[18:25], 0, v209, v208 op_sel_hi:[0,0,0]
	v_mfma_scale_f32_16x16x128_f8f6f4 v[134:137], v[2:9], v[34:41], 0, v209, v208 op_sel_hi:[0,0,0]
	v_mfma_scale_f32_16x16x128_f8f6f4 v[122:125], v[10:17], v[34:41], 0, v209, v208 op_sel_hi:[0,0,0]
	s_setprio 1
	s_waitcnt lgkmcnt(0)
	v_mfma_scale_f32_16x16x128_f8f6f4 v[158:161], v[138:145], v[26:33], 0, v209, v208 op_sel_hi:[0,0,0]
	v_mfma_scale_f32_16x16x128_f8f6f4 v[154:157], v[214:221], v[26:33], 0, v209, v208 op_sel_hi:[0,0,0]
	ds_read_b128 v[30:33], v207 offset:18432
	ds_read_b128 v[26:29], v206 offset:18432
	v_mfma_scale_f32_16x16x128_f8f6f4 v[150:153], v[138:145], v[18:25], 0, v209, v208 op_sel_hi:[0,0,0]
	v_mfma_scale_f32_16x16x128_f8f6f4 v[146:149], v[214:221], v[18:25], 0, v209, v208 op_sel_hi:[0,0,0]
	ds_read_b128 v[22:25], v207 offset:16384
	ds_read_b128 v[18:21], v206 offset:16384
	v_mfma_scale_f32_16x16x128_f8f6f4 v[130:133], v[138:145], v[42:49], 0, v209, v208 op_sel_hi:[0,0,0]
	v_mfma_scale_f32_16x16x128_f8f6f4 v[126:129], v[214:221], v[42:49], 0, v209, v208 op_sel_hi:[0,0,0]
	ds_read_b128 v[46:49], v207 offset:22528
	ds_read_b128 v[42:45], v206 offset:22528
	v_mfma_scale_f32_16x16x128_f8f6f4 v[118:121], v[138:145], v[34:41], 0, v209, v208 op_sel_hi:[0,0,0]
	v_mfma_scale_f32_16x16x128_f8f6f4 v[114:117], v[214:221], v[34:41], 0, v209, v208 op_sel_hi:[0,0,0]
	ds_read_b128 v[38:41], v207 offset:20480
	ds_read_b128 v[34:37], v206 offset:20480
	s_setprio 0
	s_mov_b32 m0, s4
	s_barrier
	global_load_lds_dwordx4 v184, s[28:29]
	s_mov_b32 m0, s33
	v_mov_b32_e32 v191, v185
	global_load_lds_dwordx4 v190, s[28:29]
	s_barrier
	s_waitcnt lgkmcnt(0)
	v_lshl_add_u64 v[242:243], s[28:29], 0, v[184:185]
	v_lshl_add_u64 v[244:245], s[28:29], 0, v[190:191]
	s_setprio 1
	s_waitcnt lgkmcnt(0)
	v_mfma_scale_f32_16x16x128_f8f6f4 v[110:113], v[2:9], v[18:25], 0, v209, v208 op_sel_hi:[0,0,0]
	v_mfma_scale_f32_16x16x128_f8f6f4 v[106:109], v[10:17], v[18:25], 0, v209, v208 op_sel_hi:[0,0,0]
	v_mfma_scale_f32_16x16x128_f8f6f4 v[102:105], v[2:9], v[26:33], 0, v209, v208 op_sel_hi:[0,0,0]
	v_mfma_scale_f32_16x16x128_f8f6f4 v[98:101], v[10:17], v[26:33], 0, v209, v208 op_sel_hi:[0,0,0]
	v_mfma_scale_f32_16x16x128_f8f6f4 v[78:81], v[2:9], v[34:41], 0, v209, v208 op_sel_hi:[0,0,0]
	v_mfma_scale_f32_16x16x128_f8f6f4 v[74:77], v[10:17], v[34:41], 0, v209, v208 op_sel_hi:[0,0,0]
	v_mfma_scale_f32_16x16x128_f8f6f4 v[70:73], v[2:9], v[42:49], 0, v209, v208 op_sel_hi:[0,0,0]
	v_mfma_scale_f32_16x16x128_f8f6f4 v[66:69], v[10:17], v[42:49], 0, v209, v208 op_sel_hi:[0,0,0]
	s_setprio 0
	s_barrier
	s_add_u32 s26, s22, 0x10000
	s_addc_u32 s27, s23, 0
	s_mov_b32 m0, s48
	v_lshl_add_u64 v[2:3], s[26:27], 0, v[188:189]
	global_load_lds_dwordx4 v[2:3], off
	v_lshl_add_u64 v[2:3], s[26:27], 0, v[186:187]
	s_mov_b32 m0, s49
	s_nop 0
	global_load_lds_dwordx4 v[2:3], off
	s_waitcnt vmcnt(6)
	s_barrier
	s_setprio 1
	v_mfma_scale_f32_16x16x128_f8f6f4 v[94:97], v[138:145], v[18:25], 0, v209, v208 op_sel_hi:[0,0,0]
	v_add_u32_e32 v14, s50, v203
	v_add_u32_e32 v6, s50, v202
	ds_read_b128 v[10:13], v6 offset:2048
	ds_read_b128 v[2:5], v6
	ds_read_b128 v[6:9], v14
	ds_read_b128 v[14:17], v14 offset:2048
	v_mfma_scale_f32_16x16x128_f8f6f4 v[90:93], v[214:221], v[18:25], 0, v209, v208 op_sel_hi:[0,0,0]
	ds_read_b128 v[22:25], v207 offset:32768
	ds_read_b128 v[18:21], v206 offset:32768
	v_mfma_scale_f32_16x16x128_f8f6f4 v[86:89], v[138:145], v[26:33], 0, v209, v208 op_sel_hi:[0,0,0]
	v_mfma_scale_f32_16x16x128_f8f6f4 v[82:85], v[214:221], v[26:33], 0, v209, v208 op_sel_hi:[0,0,0]
	ds_read_b128 v[30:33], v207 offset:34816
	ds_read_b128 v[26:29], v206 offset:34816
	v_mfma_scale_f32_16x16x128_f8f6f4 v[62:65], v[138:145], v[34:41], 0, v209, v208 op_sel_hi:[0,0,0]
	v_mfma_scale_f32_16x16x128_f8f6f4 v[58:61], v[214:221], v[34:41], 0, v209, v208 op_sel_hi:[0,0,0]
	ds_read_b128 v[38:41], v207 offset:36864
	ds_read_b128 v[34:37], v206 offset:36864
	v_mfma_scale_f32_16x16x128_f8f6f4 v[230:233], v[138:145], v[42:49], 0, v209, v208 op_sel_hi:[0,0,0]
	v_mfma_scale_f32_16x16x128_f8f6f4 v[234:237], v[214:221], v[42:49], 0, v209, v208 op_sel_hi:[0,0,0]
	ds_read_b128 v[46:49], v207 offset:38912
	ds_read_b128 v[42:45], v206 offset:38912
	s_setprio 0
	s_barrier
	s_mov_b32 m0, s34
	v_lshl_add_u64 v[50:51], s[28:29], 0, v[192:193]
	global_load_lds_dwordx4 v[50:51], off
	v_lshl_add_u64 v[50:51], s[28:29], 0, v[194:195]
	s_mov_b32 m0, s35
	s_nop 0
	global_load_lds_dwordx4 v[50:51], off
	s_waitcnt lgkmcnt(8)
	s_barrier
	s_waitcnt lgkmcnt(0)
	s_setprio 1
	s_waitcnt lgkmcnt(0)
	v_mfma_scale_f32_16x16x128_f8f6f4 v[174:177], v[2:9], v[18:25], v[174:177], v209, v208 op_sel_hi:[0,0,0]
	v_add_u32_e32 v191, s51, v203
	ds_read_b128 v[218:221], v191 offset:2048
	v_add_u32_e32 v54, s51, v202
	ds_read_b128 v[214:217], v54 offset:2048
	ds_read_b128 v[50:53], v54
	ds_read_b128 v[54:57], v191
	v_mfma_scale_f32_16x16x128_f8f6f4 v[170:173], v[10:17], v[18:25], v[170:173], v209, v208 op_sel_hi:[0,0,0]
	v_mfma_scale_f32_16x16x128_f8f6f4 v[166:169], v[2:9], v[26:33], v[166:169], v209, v208 op_sel_hi:[0,0,0]
	v_mfma_scale_f32_16x16x128_f8f6f4 v[162:165], v[10:17], v[26:33], v[162:165], v209, v208 op_sel_hi:[0,0,0]
	v_mfma_scale_f32_16x16x128_f8f6f4 v[142:145], v[2:9], v[34:41], v[222:225], v209, v208 op_sel_hi:[0,0,0]
	v_mfma_scale_f32_16x16x128_f8f6f4 v[138:141], v[10:17], v[34:41], v[226:229], v209, v208 op_sel_hi:[0,0,0]
	v_mfma_scale_f32_16x16x128_f8f6f4 v[134:137], v[2:9], v[42:49], v[134:137], v209, v208 op_sel_hi:[0,0,0]
	v_mfma_scale_f32_16x16x128_f8f6f4 v[122:125], v[10:17], v[42:49], v[122:125], v209, v208 op_sel_hi:[0,0,0]
	s_setprio 0
	s_barrier
	s_mov_b32 m0, s52
	v_lshl_add_u64 v[222:223], v[238:239], 0, s[8:9]
	global_load_lds_dwordx4 v[222:223], off
	v_lshl_add_u64 v[222:223], v[240:241], 0, s[8:9]
	s_mov_b32 m0, s53
	s_nop 0
	global_load_lds_dwordx4 v[222:223], off
	s_barrier
	s_waitcnt lgkmcnt(0)
	s_setprio 1
	s_waitcnt lgkmcnt(0)
	v_mfma_scale_f32_16x16x128_f8f6f4 v[158:161], v[50:57], v[18:25], v[158:161], v209, v208 op_sel_hi:[0,0,0]
	v_mfma_scale_f32_16x16x128_f8f6f4 v[154:157], v[214:221], v[18:25], v[154:157], v209, v208 op_sel_hi:[0,0,0]
	ds_read_b128 v[22:25], v207 offset:49152
	ds_read_b128 v[18:21], v206 offset:49152
	v_mfma_scale_f32_16x16x128_f8f6f4 v[150:153], v[50:57], v[26:33], v[150:153], v209, v208 op_sel_hi:[0,0,0]
	v_mfma_scale_f32_16x16x128_f8f6f4 v[146:149], v[214:221], v[26:33], v[146:149], v209, v208 op_sel_hi:[0,0,0]
	ds_read_b128 v[30:33], v207 offset:51200
	ds_read_b128 v[26:29], v206 offset:51200
	v_mfma_scale_f32_16x16x128_f8f6f4 v[130:133], v[50:57], v[34:41], v[130:133], v209, v208 op_sel_hi:[0,0,0]
	v_mfma_scale_f32_16x16x128_f8f6f4 v[126:129], v[214:221], v[34:41], v[126:129], v209, v208 op_sel_hi:[0,0,0]
	ds_read_b128 v[38:41], v207 offset:53248
	ds_read_b128 v[34:37], v206 offset:53248
	v_mfma_scale_f32_16x16x128_f8f6f4 v[118:121], v[50:57], v[42:49], v[118:121], v209, v208 op_sel_hi:[0,0,0]
	v_mfma_scale_f32_16x16x128_f8f6f4 v[114:117], v[214:221], v[42:49], v[114:117], v209, v208 op_sel_hi:[0,0,0]
	ds_read_b128 v[46:49], v207 offset:55296
	ds_read_b128 v[42:45], v206 offset:55296
	s_setprio 0
	s_mov_b32 m0, s38
	v_lshl_add_u64 v[222:223], v[242:243], 0, s[8:9]
	s_barrier
	global_load_lds_dwordx4 v[222:223], off
	v_lshl_add_u64 v[222:223], v[244:245], 0, s[8:9]
	s_mov_b32 m0, s39
	s_nop 0
	global_load_lds_dwordx4 v[222:223], off
	s_barrier
	s_waitcnt lgkmcnt(0)
	s_setprio 1
	s_waitcnt lgkmcnt(0)
	v_mfma_scale_f32_16x16x128_f8f6f4 v[110:113], v[2:9], v[18:25], v[110:113], v209, v208 op_sel_hi:[0,0,0]
	v_mfma_scale_f32_16x16x128_f8f6f4 v[106:109], v[10:17], v[18:25], v[106:109], v209, v208 op_sel_hi:[0,0,0]
	v_mfma_scale_f32_16x16x128_f8f6f4 v[102:105], v[2:9], v[26:33], v[102:105], v209, v208 op_sel_hi:[0,0,0]
	v_mfma_scale_f32_16x16x128_f8f6f4 v[98:101], v[10:17], v[26:33], v[98:101], v209, v208 op_sel_hi:[0,0,0]
	v_mfma_scale_f32_16x16x128_f8f6f4 v[78:81], v[2:9], v[34:41], v[78:81], v209, v208 op_sel_hi:[0,0,0]
	v_mfma_scale_f32_16x16x128_f8f6f4 v[74:77], v[10:17], v[34:41], v[74:77], v209, v208 op_sel_hi:[0,0,0]
	v_mfma_scale_f32_16x16x128_f8f6f4 v[70:73], v[2:9], v[42:49], v[70:73], v209, v208 op_sel_hi:[0,0,0]
	v_mfma_scale_f32_16x16x128_f8f6f4 v[66:69], v[10:17], v[42:49], v[66:69], v209, v208 op_sel_hi:[0,0,0]
	s_setprio 0
	s_barrier
	s_add_u32 s22, s22, 0x10080
	s_addc_u32 s23, s23, 0
	s_mov_b32 m0, s54
	v_lshl_add_u64 v[2:3], s[22:23], 0, v[188:189]
	global_load_lds_dwordx4 v[2:3], off
	v_lshl_add_u64 v[2:3], s[22:23], 0, v[186:187]
	s_add_i32 m0, s54, 0x2000
	s_nop 0
	global_load_lds_dwordx4 v[2:3], off
	s_waitcnt vmcnt(6)
	s_barrier
	s_setprio 1
	v_mfma_scale_f32_16x16x128_f8f6f4 v[94:97], v[50:57], v[18:25], v[94:97], v209, v208 op_sel_hi:[0,0,0]
	v_mfma_scale_f32_16x16x128_f8f6f4 v[90:93], v[214:221], v[18:25], v[90:93], v209, v208 op_sel_hi:[0,0,0]
	v_mfma_scale_f32_16x16x128_f8f6f4 v[86:89], v[50:57], v[26:33], v[86:89], v209, v208 op_sel_hi:[0,0,0]
	v_mfma_scale_f32_16x16x128_f8f6f4 v[82:85], v[214:221], v[26:33], v[82:85], v209, v208 op_sel_hi:[0,0,0]
	v_mfma_scale_f32_16x16x128_f8f6f4 v[62:65], v[50:57], v[34:41], v[62:65], v209, v208 op_sel_hi:[0,0,0]
	v_mfma_scale_f32_16x16x128_f8f6f4 v[58:61], v[214:221], v[34:41], v[58:61], v209, v208 op_sel_hi:[0,0,0]
	v_mfma_scale_f32_16x16x128_f8f6f4 v[54:57], v[50:57], v[42:49], v[230:233], v209, v208 op_sel_hi:[0,0,0]
	v_mfma_scale_f32_16x16x128_f8f6f4 v[50:53], v[214:221], v[42:49], v[234:237], v209, v208 op_sel_hi:[0,0,0]
	s_setprio 0
	s_cmp_ge_i32 s59, s1
	s_barrier
	s_cbranch_scc1 .LBB0_1668
	s_mov_b64 s[22:23], s[24:25]
	s_branch .LBB0_1673

.LBB0_1675:
	s_add_i32 s59, s59, 2
	s_add_u32 s24, s22, 0x100
	s_addc_u32 s25, s23, 0
	s_and_b64 s[28:29], s[26:27], exec
	s_cselect_b32 s28, 0, s24
	s_cselect_b32 s29, 0, s25
	s_add_u32 s28, s12, s28
	s_addc_u32 s29, s13, s29
	s_add_u32 s60, s57, s22
	s_addc_u32 s61, s58, s23
	s_and_b64 s[22:23], s[26:27], exec
	s_cselect_b32 s23, s55, s61
	s_cselect_b32 s22, s56, s60
	s_mov_b32 m0, s5
	s_waitcnt lgkmcnt(0)
	v_mfma_scale_f32_16x16x128_f8f6f4 v[222:225], v[2:9], v[42:49], v[142:145], v209, v208 op_sel_hi:[0,0,0]
	v_lshl_add_u64 v[238:239], s[22:23], 0, v[188:189]
	v_add_u32_e32 v191, s46, v203
	v_lshl_add_u64 v[240:241], s[22:23], 0, v[186:187]
	v_mov_b32_e32 v193, v185
	v_mov_b32_e32 v195, v185
	s_nop 1
	v_add_u32_e32 v142, s46, v202
	v_mfma_scale_f32_16x16x128_f8f6f4 v[226:229], v[10:17], v[42:49], v[138:141], v209, v208 op_sel_hi:[0,0,0]
	s_nop 6
	ds_read_b128 v[138:141], v142
	ds_read_b128 v[214:217], v142 offset:2048
	ds_read_b128 v[142:145], v191
	ds_read_b128 v[218:221], v191 offset:2048
	global_load_lds_dwordx4 v[238:239], off
	s_mov_b32 m0, s31
	s_nop 0
	global_load_lds_dwordx4 v[240:241], off
	v_mfma_scale_f32_16x16x128_f8f6f4 v[174:177], v[2:9], v[26:33], v[174:177], v209, v208 op_sel_hi:[0,0,0]
	s_barrier
	s_waitcnt lgkmcnt(0)
	v_mfma_scale_f32_16x16x128_f8f6f4 v[170:173], v[10:17], v[26:33], v[170:173], v209, v208 op_sel_hi:[0,0,0]
	v_mfma_scale_f32_16x16x128_f8f6f4 v[166:169], v[2:9], v[18:25], v[166:169], v209, v208 op_sel_hi:[0,0,0]
	v_mfma_scale_f32_16x16x128_f8f6f4 v[162:165], v[10:17], v[18:25], v[162:165], v209, v208 op_sel_hi:[0,0,0]
	v_mfma_scale_f32_16x16x128_f8f6f4 v[134:137], v[2:9], v[34:41], v[134:137], v209, v208 op_sel_hi:[0,0,0]
	v_mfma_scale_f32_16x16x128_f8f6f4 v[122:125], v[10:17], v[34:41], v[122:125], v209, v208 op_sel_hi:[0,0,0]
	s_setprio 1
	s_waitcnt lgkmcnt(0)
	v_mfma_scale_f32_16x16x128_f8f6f4 v[158:161], v[138:145], v[26:33], v[158:161], v209, v208 op_sel_hi:[0,0,0]
	v_mfma_scale_f32_16x16x128_f8f6f4 v[154:157], v[214:221], v[26:33], v[154:157], v209, v208 op_sel_hi:[0,0,0]
	ds_read_b128 v[30:33], v207 offset:18432
	ds_read_b128 v[26:29], v206 offset:18432
	v_mfma_scale_f32_16x16x128_f8f6f4 v[150:153], v[138:145], v[18:25], v[150:153], v209, v208 op_sel_hi:[0,0,0]
	v_mfma_scale_f32_16x16x128_f8f6f4 v[146:149], v[214:221], v[18:25], v[146:149], v209, v208 op_sel_hi:[0,0,0]
	ds_read_b128 v[22:25], v207 offset:16384
	ds_read_b128 v[18:21], v206 offset:16384
	v_mfma_scale_f32_16x16x128_f8f6f4 v[130:133], v[138:145], v[42:49], v[130:133], v209, v208 op_sel_hi:[0,0,0]
	v_mfma_scale_f32_16x16x128_f8f6f4 v[126:129], v[214:221], v[42:49], v[126:129], v209, v208 op_sel_hi:[0,0,0]
	ds_read_b128 v[46:49], v207 offset:22528
	ds_read_b128 v[42:45], v206 offset:22528
	v_mfma_scale_f32_16x16x128_f8f6f4 v[118:121], v[138:145], v[34:41], v[118:121], v209, v208 op_sel_hi:[0,0,0]
	v_mfma_scale_f32_16x16x128_f8f6f4 v[114:117], v[214:221], v[34:41], v[114:117], v209, v208 op_sel_hi:[0,0,0]
	ds_read_b128 v[38:41], v207 offset:20480
	ds_read_b128 v[34:37], v206 offset:20480
	s_setprio 0
	s_mov_b32 m0, s4
	s_barrier
	global_load_lds_dwordx4 v184, s[28:29]
	s_mov_b32 m0, s33
	v_mov_b32_e32 v191, v185
	global_load_lds_dwordx4 v190, s[28:29]
	s_barrier
	s_waitcnt lgkmcnt(0)
	v_lshl_add_u64 v[242:243], s[28:29], 0, v[184:185]
	v_lshl_add_u64 v[244:245], s[28:29], 0, v[190:191]
	s_setprio 1
	s_waitcnt lgkmcnt(0)
	v_mfma_scale_f32_16x16x128_f8f6f4 v[110:113], v[2:9], v[18:25], v[110:113], v209, v208 op_sel_hi:[0,0,0]
	v_mfma_scale_f32_16x16x128_f8f6f4 v[106:109], v[10:17], v[18:25], v[106:109], v209, v208 op_sel_hi:[0,0,0]
	v_mfma_scale_f32_16x16x128_f8f6f4 v[102:105], v[2:9], v[26:33], v[102:105], v209, v208 op_sel_hi:[0,0,0]
	v_mfma_scale_f32_16x16x128_f8f6f4 v[98:101], v[10:17], v[26:33], v[98:101], v209, v208 op_sel_hi:[0,0,0]
	v_mfma_scale_f32_16x16x128_f8f6f4 v[78:81], v[2:9], v[34:41], v[78:81], v209, v208 op_sel_hi:[0,0,0]
	v_mfma_scale_f32_16x16x128_f8f6f4 v[74:77], v[10:17], v[34:41], v[74:77], v209, v208 op_sel_hi:[0,0,0]
	v_mfma_scale_f32_16x16x128_f8f6f4 v[70:73], v[2:9], v[42:49], v[70:73], v209, v208 op_sel_hi:[0,0,0]
	v_mfma_scale_f32_16x16x128_f8f6f4 v[66:69], v[10:17], v[42:49], v[66:69], v209, v208 op_sel_hi:[0,0,0]
	s_setprio 0
	s_barrier
	s_add_u32 s26, s22, 0x10000
	s_addc_u32 s27, s23, 0
	s_mov_b32 m0, s48
	v_lshl_add_u64 v[2:3], s[26:27], 0, v[188:189]
	global_load_lds_dwordx4 v[2:3], off
	v_lshl_add_u64 v[2:3], s[26:27], 0, v[186:187]
	s_mov_b32 m0, s49
	s_nop 0
	global_load_lds_dwordx4 v[2:3], off
	s_waitcnt vmcnt(6)
	s_barrier
	s_setprio 1
	v_mfma_scale_f32_16x16x128_f8f6f4 v[94:97], v[138:145], v[18:25], v[94:97], v209, v208 op_sel_hi:[0,0,0]
	v_add_u32_e32 v14, s50, v203
	v_add_u32_e32 v6, s50, v202
	ds_read_b128 v[10:13], v6 offset:2048
	ds_read_b128 v[2:5], v6
	ds_read_b128 v[6:9], v14
	ds_read_b128 v[14:17], v14 offset:2048
	v_mfma_scale_f32_16x16x128_f8f6f4 v[90:93], v[214:221], v[18:25], v[90:93], v209, v208 op_sel_hi:[0,0,0]
	ds_read_b128 v[22:25], v207 offset:32768
	ds_read_b128 v[18:21], v206 offset:32768
	v_mfma_scale_f32_16x16x128_f8f6f4 v[86:89], v[138:145], v[26:33], v[86:89], v209, v208 op_sel_hi:[0,0,0]
	v_mfma_scale_f32_16x16x128_f8f6f4 v[82:85], v[214:221], v[26:33], v[82:85], v209, v208 op_sel_hi:[0,0,0]
	ds_read_b128 v[30:33], v207 offset:34816
	ds_read_b128 v[26:29], v206 offset:34816
	v_mfma_scale_f32_16x16x128_f8f6f4 v[62:65], v[138:145], v[34:41], v[62:65], v209, v208 op_sel_hi:[0,0,0]
	v_mfma_scale_f32_16x16x128_f8f6f4 v[58:61], v[214:221], v[34:41], v[58:61], v209, v208 op_sel_hi:[0,0,0]
	ds_read_b128 v[38:41], v207 offset:36864
	ds_read_b128 v[34:37], v206 offset:36864
	v_mfma_scale_f32_16x16x128_f8f6f4 v[230:233], v[138:145], v[42:49], v[54:57], v209, v208 op_sel_hi:[0,0,0]
	v_mfma_scale_f32_16x16x128_f8f6f4 v[234:237], v[214:221], v[42:49], v[50:53], v209, v208 op_sel_hi:[0,0,0]
	ds_read_b128 v[46:49], v207 offset:38912
	ds_read_b128 v[42:45], v206 offset:38912
	s_setprio 0
	s_barrier
	s_mov_b32 m0, s34
	v_lshl_add_u64 v[50:51], s[28:29], 0, v[192:193]
	global_load_lds_dwordx4 v[50:51], off
	v_lshl_add_u64 v[50:51], s[28:29], 0, v[194:195]
	s_mov_b32 m0, s35
	s_nop 0
	global_load_lds_dwordx4 v[50:51], off
	s_waitcnt lgkmcnt(8)
	s_barrier
	s_waitcnt lgkmcnt(0)
	s_setprio 1
	s_waitcnt lgkmcnt(0)
	v_mfma_scale_f32_16x16x128_f8f6f4 v[174:177], v[2:9], v[18:25], v[174:177], v209, v208 op_sel_hi:[0,0,0]
	v_add_u32_e32 v191, s51, v203
	ds_read_b128 v[218:221], v191 offset:2048
	v_add_u32_e32 v54, s51, v202
	ds_read_b128 v[214:217], v54 offset:2048
	ds_read_b128 v[50:53], v54
	ds_read_b128 v[54:57], v191
	v_mfma_scale_f32_16x16x128_f8f6f4 v[170:173], v[10:17], v[18:25], v[170:173], v209, v208 op_sel_hi:[0,0,0]
	v_mfma_scale_f32_16x16x128_f8f6f4 v[166:169], v[2:9], v[26:33], v[166:169], v209, v208 op_sel_hi:[0,0,0]
	v_mfma_scale_f32_16x16x128_f8f6f4 v[162:165], v[10:17], v[26:33], v[162:165], v209, v208 op_sel_hi:[0,0,0]
	v_mfma_scale_f32_16x16x128_f8f6f4 v[142:145], v[2:9], v[34:41], v[222:225], v209, v208 op_sel_hi:[0,0,0]
	v_mfma_scale_f32_16x16x128_f8f6f4 v[138:141], v[10:17], v[34:41], v[226:229], v209, v208 op_sel_hi:[0,0,0]
	v_mfma_scale_f32_16x16x128_f8f6f4 v[134:137], v[2:9], v[42:49], v[134:137], v209, v208 op_sel_hi:[0,0,0]
	v_mfma_scale_f32_16x16x128_f8f6f4 v[122:125], v[10:17], v[42:49], v[122:125], v209, v208 op_sel_hi:[0,0,0]
	s_setprio 0
	s_barrier
	s_mov_b32 m0, s52
	v_lshl_add_u64 v[222:223], v[238:239], 0, s[8:9]
	global_load_lds_dwordx4 v[222:223], off
	v_lshl_add_u64 v[222:223], v[240:241], 0, s[8:9]
	s_mov_b32 m0, s53
	s_nop 0
	global_load_lds_dwordx4 v[222:223], off
	s_barrier
	s_waitcnt lgkmcnt(0)
	s_setprio 1
	s_waitcnt lgkmcnt(0)
	v_mfma_scale_f32_16x16x128_f8f6f4 v[158:161], v[50:57], v[18:25], v[158:161], v209, v208 op_sel_hi:[0,0,0]
	v_mfma_scale_f32_16x16x128_f8f6f4 v[154:157], v[214:221], v[18:25], v[154:157], v209, v208 op_sel_hi:[0,0,0]
	ds_read_b128 v[22:25], v207 offset:49152
	ds_read_b128 v[18:21], v206 offset:49152
	v_mfma_scale_f32_16x16x128_f8f6f4 v[150:153], v[50:57], v[26:33], v[150:153], v209, v208 op_sel_hi:[0,0,0]
	v_mfma_scale_f32_16x16x128_f8f6f4 v[146:149], v[214:221], v[26:33], v[146:149], v209, v208 op_sel_hi:[0,0,0]
	ds_read_b128 v[30:33], v207 offset:51200
	ds_read_b128 v[26:29], v206 offset:51200
	v_mfma_scale_f32_16x16x128_f8f6f4 v[130:133], v[50:57], v[34:41], v[130:133], v209, v208 op_sel_hi:[0,0,0]
	v_mfma_scale_f32_16x16x128_f8f6f4 v[126:129], v[214:221], v[34:41], v[126:129], v209, v208 op_sel_hi:[0,0,0]
	ds_read_b128 v[38:41], v207 offset:53248
	ds_read_b128 v[34:37], v206 offset:53248
	v_mfma_scale_f32_16x16x128_f8f6f4 v[118:121], v[50:57], v[42:49], v[118:121], v209, v208 op_sel_hi:[0,0,0]
	v_mfma_scale_f32_16x16x128_f8f6f4 v[114:117], v[214:221], v[42:49], v[114:117], v209, v208 op_sel_hi:[0,0,0]
	ds_read_b128 v[46:49], v207 offset:55296
	ds_read_b128 v[42:45], v206 offset:55296
	s_setprio 0
	s_mov_b32 m0, s38
	v_lshl_add_u64 v[222:223], v[242:243], 0, s[8:9]
	s_barrier
	global_load_lds_dwordx4 v[222:223], off
	v_lshl_add_u64 v[222:223], v[244:245], 0, s[8:9]
	s_mov_b32 m0, s39
	s_nop 0
	global_load_lds_dwordx4 v[222:223], off
	s_barrier
	s_waitcnt lgkmcnt(0)
	s_setprio 1
	s_waitcnt lgkmcnt(0)
	v_mfma_scale_f32_16x16x128_f8f6f4 v[110:113], v[2:9], v[18:25], v[110:113], v209, v208 op_sel_hi:[0,0,0]
	v_mfma_scale_f32_16x16x128_f8f6f4 v[106:109], v[10:17], v[18:25], v[106:109], v209, v208 op_sel_hi:[0,0,0]
	v_mfma_scale_f32_16x16x128_f8f6f4 v[102:105], v[2:9], v[26:33], v[102:105], v209, v208 op_sel_hi:[0,0,0]
	v_mfma_scale_f32_16x16x128_f8f6f4 v[98:101], v[10:17], v[26:33], v[98:101], v209, v208 op_sel_hi:[0,0,0]
	v_mfma_scale_f32_16x16x128_f8f6f4 v[78:81], v[2:9], v[34:41], v[78:81], v209, v208 op_sel_hi:[0,0,0]
	v_mfma_scale_f32_16x16x128_f8f6f4 v[74:77], v[10:17], v[34:41], v[74:77], v209, v208 op_sel_hi:[0,0,0]
	v_mfma_scale_f32_16x16x128_f8f6f4 v[70:73], v[2:9], v[42:49], v[70:73], v209, v208 op_sel_hi:[0,0,0]
	v_mfma_scale_f32_16x16x128_f8f6f4 v[66:69], v[10:17], v[42:49], v[66:69], v209, v208 op_sel_hi:[0,0,0]
	s_setprio 0
	s_barrier
	s_add_u32 s22, s22, 0x10080
	s_addc_u32 s23, s23, 0
	s_mov_b32 m0, s54
	v_lshl_add_u64 v[2:3], s[22:23], 0, v[188:189]
	global_load_lds_dwordx4 v[2:3], off
	v_lshl_add_u64 v[2:3], s[22:23], 0, v[186:187]
	s_add_i32 m0, s54, 0x2000
	s_nop 0
	global_load_lds_dwordx4 v[2:3], off
	s_waitcnt vmcnt(6)
	s_barrier
	s_setprio 1
	v_mfma_scale_f32_16x16x128_f8f6f4 v[94:97], v[50:57], v[18:25], v[94:97], v209, v208 op_sel_hi:[0,0,0]
	v_mfma_scale_f32_16x16x128_f8f6f4 v[90:93], v[214:221], v[18:25], v[90:93], v209, v208 op_sel_hi:[0,0,0]
	v_mfma_scale_f32_16x16x128_f8f6f4 v[86:89], v[50:57], v[26:33], v[86:89], v209, v208 op_sel_hi:[0,0,0]
	v_mfma_scale_f32_16x16x128_f8f6f4 v[82:85], v[214:221], v[26:33], v[82:85], v209, v208 op_sel_hi:[0,0,0]
	v_mfma_scale_f32_16x16x128_f8f6f4 v[62:65], v[50:57], v[34:41], v[62:65], v209, v208 op_sel_hi:[0,0,0]
	v_mfma_scale_f32_16x16x128_f8f6f4 v[58:61], v[214:221], v[34:41], v[58:61], v209, v208 op_sel_hi:[0,0,0]
	v_mfma_scale_f32_16x16x128_f8f6f4 v[54:57], v[50:57], v[42:49], v[230:233], v209, v208 op_sel_hi:[0,0,0]
	v_mfma_scale_f32_16x16x128_f8f6f4 v[50:53], v[214:221], v[42:49], v[234:237], v209, v208 op_sel_hi:[0,0,0]
	s_setprio 0
	s_cmp_ge_i32 s59, s1
	s_barrier
	s_cbranch_scc1 .LBB0_1668
	s_mov_b64 s[22:23], s[24:25]
	s_branch .LBB0_1673
